# gate/up extra-row instance: first-half A fragments in own registers, requested one step ahead; second halves waited before sub-step 2
# speedup vs baseline: 1.0074x; 1.0074x over previous
.LBB0_1302:
	s_or_b64 exec, exec, s[0:1]
	s_add_i32 s0, s29, 0xfffffdbf
	v_lshl_add_u32 v2, v2, 2, 0
	v_mov_b32_e32 v235, v231
	s_cmp_lt_u32 s0, 0xffffffc0
	s_waitcnt vmcnt(0)
	ds_write_b32 v2, v0 offset:57344
	s_waitcnt lgkmcnt(0)
	s_barrier
	s_cselect_b64 s[0:1], -1, 0
	v_and_b32_e32 v234, 31, v235
	s_or_b64 s[42:43], s[68:69], s[0:1]
	v_and_b32_e32 v233, 32, v235
	v_and_b32_e32 v0, 7, v235
	v_mul_u32_u24_e32 v2, 0x48, v234
	s_mov_b64 s[0:1], -1
	s_and_b64 vcc, exec, s[42:43]
	v_lshlrev_b32_e32 v237, 4, v0
	v_or_b32_e32 v236, s28, v0
	v_add_lshl_u32 v232, v2, v233, 1
	s_cbranch_vccnz .LBB0_1320
	v_lshrrev_b32_e32 v0, 2, v235
	v_readlane_b32 s0, v255, 5
	v_mov_b32_e32 v240, v232
	v_readlane_b32 s1, v255, 9
	v_and_or_b32 v0, v0, 14, s0
	s_movk_i32 s0, 0x48
	v_mul_lo_u32 v2, v236, s0
	v_lshl_or_b32 v238, v0, 10, v237
	v_add_lshl_u32 v239, v2, v0, 1
	v_lshlrev_b32_e32 v0, 2, v234
	v_readlane_b32 s0, v255, 7
	s_mov_b64 s[42:43], s[36:37]
	v_add_u32_e32 v244, 0, v239
	v_add_u32_e32 v2, s0, v0
	v_add_u32_e32 v2, 0xd800, v2
	ds_read2_b32 v[2:3], v2 offset1:32
	s_mov_b32 s0, 0x24000
	v_add_u32_e32 v0, s1, v0
	s_cmp_lt_i32 s83, s29
	v_add_u32_e32 v245, 0, v240
	s_waitcnt lgkmcnt(0)
	v_lshlrev_b32_e32 v4, 7, v2
	v_and_b32_e32 v4, 0xfffffc00, v4
	v_cmp_ne_u32_e32 vcc, s0, v2
	s_mov_b32 s2, 0
	v_add_u32_e32 v246, s33, v245
	v_cndmask_b32_e32 v2, 0, v4, vcc
	v_or_b32_e32 v241, v2, v233
	v_lshlrev_b32_e32 v2, 7, v3
	v_and_b32_e32 v2, 0xfffffc00, v2
	v_cmp_ne_u32_e32 vcc, s0, v3
	s_movk_i32 s49, 0x80
	s_mov_b32 s39, 0
	v_cndmask_b32_e32 v2, 0, v2, vcc
	v_or_b32_e32 v242, v2, v233
	global_load_dwordx4 v[204:207], v241, s[54:55] offset:16
	global_load_dwordx4 v[220:223], v241, s[54:55]
	global_load_dwordx4 v[192:195], v242, s[54:55] offset:16
	global_load_dwordx4 v[224:227], v242, s[54:55]
	ds_read_b32 v0, v0 offset:57344
	s_waitcnt lgkmcnt(0)
	v_lshlrev_b32_e32 v2, 7, v0
	v_and_b32_e32 v2, 0xfffffc00, v2
	v_cmp_ne_u32_e32 vcc, s0, v0
	s_mov_b64 s[0:1], s[34:35]
	s_nop 0
	v_cndmask_b32_e32 v0, 0, v2, vcc
	v_or_b32_e32 v243, v0, v233
	v_mov_b32_e32 v0, v238
	global_load_dwordx4 v[200:203], v243, s[54:55] offset:16
	global_load_dwordx4 v[196:199], v243, s[54:55]
	global_load_dwordx4 v[2:5], v0, s[0:1] nt
	global_load_dwordx4 v[6:9], v0, s[0:1] offset:1024 nt
	global_load_dwordx4 v[10:13], v0, s[42:43] nt
	global_load_dwordx4 v[14:17], v0, s[42:43] offset:1024 nt
	s_mov_b64 s[0:1], s[92:93]
	s_mov_b64 s[42:43], s[96:97]
	v_mov_b32_e32 v0, v238
	global_load_dwordx4 v[160:163], v0, s[42:43] nt
	global_load_dwordx4 v[164:167], v0, s[42:43] offset:1024 nt
	global_load_dwordx4 v[168:171], v0, s[0:1] nt
	global_load_dwordx4 v[172:175], v0, s[0:1] offset:1024 nt
	s_mov_b64 s[42:43], s[88:89]
	s_mov_b64 s[0:1], s[8:9]
	s_waitcnt vmcnt(6)
	v_cvt_pk_bf16_f32 v0, v2, v6
	v_mov_b32_e32 v6, v1
	s_waitcnt vmcnt(4)
	v_cvt_pk_bf16_f32 v2, v10, v14
	ds_write2_b32 v244, v0, v2 offset1:8
	v_cvt_pk_bf16_f32 v0, v3, v7
	v_cvt_pk_bf16_f32 v2, v11, v15
	v_add_u32_e32 v3, 0x400, v244
	ds_write2_b32 v3, v0, v2 offset0:32 offset1:40
	v_cvt_pk_bf16_f32 v0, v4, v8
	v_cvt_pk_bf16_f32 v2, v12, v16
	v_add_u32_e32 v3, 0x800, v244
	ds_write2_b32 v3, v0, v2 offset0:64 offset1:72
	v_cvt_pk_bf16_f32 v0, v5, v9
	v_cvt_pk_bf16_f32 v2, v13, v17
	v_add_u32_e32 v3, 0xc00, v244
	ds_write2_b32 v3, v0, v2 offset0:96 offset1:104
	v_mov_b32_e32 v0, v238
	global_load_dwordx4 v[176:179], v0, s[42:43] nt
	global_load_dwordx4 v[180:183], v0, s[42:43] offset:1024 nt
	global_load_dwordx4 v[184:187], v0, s[0:1] nt
	global_load_dwordx4 v[188:191], v0, s[0:1] offset:1024 nt
	v_mov_b32_e32 v14, v1
	v_mov_b32_e32 v15, v1
	s_cselect_b64 s[0:1], -1, 0
	v_mov_b32_e32 v0, v1
	v_mov_b32_e32 v2, v1
	v_mov_b32_e32 v3, v1
	v_mov_b32_e32 v4, v1
	v_mov_b32_e32 v5, v1
	v_mov_b32_e32 v7, v1
	v_mov_b32_e32 v8, v1
	v_mov_b32_e32 v9, v1
	v_mov_b32_e32 v10, v1
	v_mov_b32_e32 v11, v1
	v_mov_b32_e32 v12, v1
	v_mov_b32_e32 v13, v1
	v_mov_b32_e32 v16, 0
	s_cmp_lt_i32 s80, s29
	v_mov_b64_e32 v[46:47], v[14:15]
	v_mov_b64_e32 v[78:79], v[14:15]
	v_mov_b64_e32 v[62:63], v[14:15]
	v_mov_b64_e32 v[94:95], v[14:15]
	v_mov_b64_e32 v[110:111], v[14:15]
	v_mov_b64_e32 v[142:143], v[14:15]
	v_mov_b64_e32 v[126:127], v[14:15]
	v_mov_b64_e32 v[158:159], v[14:15]
	s_cselect_b64 s[44:45], -1, 0
	v_mov_b64_e32 v[44:45], v[12:13]
	v_mov_b64_e32 v[42:43], v[10:11]
	v_mov_b64_e32 v[40:41], v[8:9]
	v_mov_b64_e32 v[38:39], v[6:7]
	v_mov_b64_e32 v[36:37], v[4:5]
	v_mov_b64_e32 v[34:35], v[2:3]
	v_mov_b64_e32 v[32:33], v[0:1]
	v_mov_b64_e32 v[76:77], v[12:13]
	v_mov_b64_e32 v[74:75], v[10:11]
	v_mov_b64_e32 v[72:73], v[8:9]
	v_mov_b64_e32 v[70:71], v[6:7]
	v_mov_b64_e32 v[68:69], v[4:5]
	v_mov_b64_e32 v[66:67], v[2:3]
	v_mov_b64_e32 v[64:65], v[0:1]
	v_mov_b64_e32 v[60:61], v[12:13]
	v_mov_b64_e32 v[58:59], v[10:11]
	v_mov_b64_e32 v[56:57], v[8:9]
	v_mov_b64_e32 v[54:55], v[6:7]
	v_mov_b64_e32 v[52:53], v[4:5]
	v_mov_b64_e32 v[50:51], v[2:3]
	v_mov_b64_e32 v[48:49], v[0:1]
	v_mov_b64_e32 v[92:93], v[12:13]
	v_mov_b64_e32 v[90:91], v[10:11]
	v_mov_b64_e32 v[88:89], v[8:9]
	v_mov_b64_e32 v[86:87], v[6:7]
	v_mov_b64_e32 v[84:85], v[4:5]
	v_mov_b64_e32 v[82:83], v[2:3]
	v_mov_b64_e32 v[80:81], v[0:1]
	v_mov_b64_e32 v[108:109], v[12:13]
	v_mov_b64_e32 v[106:107], v[10:11]
	v_mov_b64_e32 v[104:105], v[8:9]
	v_mov_b64_e32 v[102:103], v[6:7]
	v_mov_b64_e32 v[100:101], v[4:5]
	v_mov_b64_e32 v[98:99], v[2:3]
	v_mov_b64_e32 v[96:97], v[0:1]
	v_mov_b64_e32 v[140:141], v[12:13]
	v_mov_b64_e32 v[138:139], v[10:11]
	v_mov_b64_e32 v[136:137], v[8:9]
	v_mov_b64_e32 v[134:135], v[6:7]
	v_mov_b64_e32 v[132:133], v[4:5]
	v_mov_b64_e32 v[130:131], v[2:3]
	v_mov_b64_e32 v[128:129], v[0:1]
	v_mov_b64_e32 v[124:125], v[12:13]
	v_mov_b64_e32 v[122:123], v[10:11]
	v_mov_b64_e32 v[120:121], v[8:9]
	v_mov_b64_e32 v[118:119], v[6:7]
	v_mov_b64_e32 v[116:117], v[4:5]
	v_mov_b64_e32 v[114:115], v[2:3]
	v_mov_b64_e32 v[112:113], v[0:1]
	v_mov_b64_e32 v[156:157], v[12:13]
	v_mov_b64_e32 v[154:155], v[10:11]
	v_mov_b64_e32 v[152:153], v[8:9]
	v_mov_b64_e32 v[150:151], v[6:7]
	v_mov_b64_e32 v[148:149], v[4:5]
	v_mov_b64_e32 v[146:147], v[2:3]
	v_mov_b64_e32 v[144:145], v[0:1]
	v_mov_b32_e32 v17, v16
	v_mov_b32_e32 v18, v16
	v_mov_b32_e32 v19, v16
	v_mov_b32_e32 v20, v16
	v_mov_b32_e32 v21, v16
	v_mov_b32_e32 v22, v16
	v_mov_b32_e32 v23, v16
	v_mov_b32_e32 v24, v16
	v_mov_b32_e32 v25, v16
	v_mov_b32_e32 v26, v16
	v_mov_b32_e32 v27, v16
	v_mov_b32_e32 v28, v16
	v_mov_b32_e32 v29, v16
	v_mov_b32_e32 v30, v16
	v_mov_b32_e32 v31, v16
	s_branch .LBB0_1306

.LBB0_1306:
	s_add_i32 s98, s49, 0xffffff80
	s_and_b32 s98, s98, 0x380
	s_or_b32 s98, s98, 64
	s_add_u32 s98, s98, s54
	s_addc_u32 s99, 0, s55
	global_load_dwordx4 v[228:231], v241, s[98:99]
	global_load_dwordx4 v[232:235], v242, s[98:99]
	s_add_i32 s25, s2, 1
	s_cmp_lg_u32 s2, 2
	s_cselect_b32 s26, s25, 0
	s_mul_i32 s25, s26, 0x4800
	s_add_i32 s56, s25, 0
	s_add_i32 s25, s39, 3
	s_cmp_lt_u32 s39, 61
	s_cselect_b32 s25, s25, 0
	s_lshr_b32 s42, s25, 4
	s_add_i32 s42, s42, s66
	s_and_b32 s42, s42, 3
	s_add_i32 s42, s42, s27
	s_lshl_b32 s25, s25, 16
	s_lshl_b32 s42, s42, 8
	s_and_b32 s25, s25, 0xf0000
	v_add_u32_e32 v0, s56, v239
	s_cmp_lg_u32 s39, 0
	s_cbranch_scc1 .Lgx_es
	s_waitcnt vmcnt(6)
.Lgx_es:
	s_waitcnt vmcnt(12)
	v_cvt_pk_bf16_f32 v2, v160, v164
	v_cvt_pk_bf16_f32 v3, v168, v172
	s_or_b32 s25, s42, s25
	s_waitcnt lgkmcnt(0)
	s_barrier
	ds_write2_b32 v0, v2, v3 offset1:8
	v_cvt_pk_bf16_f32 v2, v161, v165
	v_cvt_pk_bf16_f32 v3, v169, v173
	v_add_u32_e32 v4, 0x400, v0
	s_add_u32 s42, s67, s25
	ds_write2_b32 v4, v2, v3 offset0:32 offset1:40
	v_cvt_pk_bf16_f32 v2, v162, v166
	v_cvt_pk_bf16_f32 v3, v170, v174
	v_add_u32_e32 v4, 0x800, v0
	s_addc_u32 s43, s38, 0
	ds_write2_b32 v4, v2, v3 offset0:64 offset1:72
	v_cvt_pk_bf16_f32 v2, v163, v167
	v_cvt_pk_bf16_f32 v3, v171, v175
	v_add_u32_e32 v0, 0xc00, v0
	s_add_u32 s46, s42, 0x4000
	ds_write2_b32 v0, v2, v3 offset0:96 offset1:104
	s_addc_u32 s47, s43, 0
	v_mov_b32_e32 v0, v238
	global_load_dwordx4 v[160:163], v0, s[42:43] nt
	global_load_dwordx4 v[164:167], v0, s[42:43] offset:1024 nt
	global_load_dwordx4 v[168:171], v0, s[46:47] nt
	global_load_dwordx4 v[172:175], v0, s[46:47] offset:1024 nt
	s_add_i32 s25, s49, 0xffffff80
	s_and_b32 s25, s25, 0x380
	s_or_b32 s25, s25, 64
	s_add_u32 s46, s25, s54
	v_cndmask_b32_e64 v0, 0, 1, s[0:1]
	s_addc_u32 s47, 0, s55
	s_mul_i32 s90, s2, 0x4800
	v_cmp_ne_u32_e64 s[42:43], 1, v0
	s_andn2_b64 vcc, exec, s[0:1]
	s_cbranch_vccnz .LBB0_1308
	s_waitcnt vmcnt(14)
	v_cvt_pk_f32_fp8_e32 v[6:7], v220
	v_cvt_pk_f32_fp8_sdwa v[8:9], v220 src0_sel:WORD_1
	v_cvt_pk_f32_fp8_e32 v[10:11], v221
	v_cvt_pk_f32_fp8_sdwa v[12:13], v221 src0_sel:WORD_1
	v_add_u32_e32 v0, s90, v245
	ds_read_b128 v[2:5], v0
	v_cvt_pk_bf16_f32 v6, v6, v7
	v_cvt_pk_bf16_f32 v7, v8, v9
	v_cvt_pk_bf16_f32 v8, v10, v11
	v_cvt_pk_bf16_f32 v9, v12, v13
	ds_read_b128 v[10:13], v0 offset:4608
	ds_read_b128 v[248:251], v0 offset:9216
	ds_read_b128 v[216:219], v0 offset:13824
	s_waitcnt lgkmcnt(3)
	v_mfma_f32_32x32x16_bf16 v[144:159], v[2:5], v[6:9], v[144:159]
	s_waitcnt vmcnt(14)
	v_cvt_pk_f32_fp8_e32 v[14:15], v225
	s_waitcnt lgkmcnt(2)
	v_mfma_f32_32x32x16_bf16 v[112:127], v[10:13], v[6:9], v[112:127]
	s_waitcnt lgkmcnt(1)
	v_mfma_f32_32x32x16_bf16 v[128:143], v[248:251], v[6:9], v[128:143]
	s_waitcnt lgkmcnt(0)
	v_mfma_f32_32x32x16_bf16 v[96:111], v[216:219], v[6:9], v[96:111]
	v_cvt_pk_f32_fp8_e32 v[6:7], v224
	v_cvt_pk_f32_fp8_sdwa v[8:9], v224 src0_sel:WORD_1
	v_cvt_pk_f32_fp8_sdwa v[208:209], v225 src0_sel:WORD_1
	v_cvt_pk_bf16_f32 v6, v6, v7
	v_cvt_pk_bf16_f32 v7, v8, v9
	v_cvt_pk_bf16_f32 v8, v14, v15
	v_cvt_pk_bf16_f32 v9, v208, v209
	v_cvt_pk_f32_fp8_e32 v[14:15], v227
	v_cvt_pk_f32_fp8_sdwa v[208:209], v227 src0_sel:WORD_1
	v_mfma_f32_32x32x16_bf16 v[80:95], v[2:5], v[6:9], v[80:95]
	ds_read_b128 v[2:5], v0 offset:16
	v_mfma_f32_32x32x16_bf16 v[48:63], v[10:13], v[6:9], v[48:63]
	v_cvt_pk_f32_fp8_e32 v[10:11], v223
	v_cvt_pk_f32_fp8_sdwa v[12:13], v223 src0_sel:WORD_1
	v_mfma_f32_32x32x16_bf16 v[64:79], v[248:251], v[6:9], v[64:79]
	v_mfma_f32_32x32x16_bf16 v[32:47], v[216:219], v[6:9], v[32:47]
	v_cvt_pk_f32_fp8_e32 v[6:7], v222
	v_cvt_pk_f32_fp8_sdwa v[8:9], v222 src0_sel:WORD_1
	ds_read_b128 v[212:215], v0 offset:9232
	ds_read_b128 v[216:219], v0 offset:13840
	v_cvt_pk_bf16_f32 v6, v6, v7
	v_cvt_pk_bf16_f32 v7, v8, v9
	v_cvt_pk_bf16_f32 v8, v10, v11
	v_cvt_pk_bf16_f32 v9, v12, v13
	ds_read_b128 v[10:13], v0 offset:4624
	s_waitcnt lgkmcnt(3)
	v_mfma_f32_32x32x16_bf16 v[144:159], v[2:5], v[6:9], v[144:159]
	s_waitcnt lgkmcnt(0)
	v_mfma_f32_32x32x16_bf16 v[112:127], v[10:13], v[6:9], v[112:127]
	v_mfma_f32_32x32x16_bf16 v[128:143], v[212:215], v[6:9], v[128:143]
	v_mfma_f32_32x32x16_bf16 v[96:111], v[216:219], v[6:9], v[96:111]
	v_cvt_pk_f32_fp8_e32 v[6:7], v226
	v_cvt_pk_f32_fp8_sdwa v[8:9], v226 src0_sel:WORD_1
	v_cvt_pk_bf16_f32 v6, v6, v7
	v_cvt_pk_bf16_f32 v7, v8, v9
	v_cvt_pk_bf16_f32 v8, v14, v15
	v_cvt_pk_bf16_f32 v9, v208, v209
	ds_read_b128 v[208:211], v0 offset:9248
	s_waitcnt vmcnt(8)
	v_cvt_pk_f32_fp8_e32 v[14:15], v193
	v_mfma_f32_32x32x16_bf16 v[80:95], v[2:5], v[6:9], v[80:95]
	ds_read_b128 v[2:5], v0 offset:32
	v_mfma_f32_32x32x16_bf16 v[48:63], v[10:13], v[6:9], v[48:63]
	v_cvt_pk_f32_fp8_e32 v[10:11], v205
	v_cvt_pk_f32_fp8_sdwa v[12:13], v205 src0_sel:WORD_1
	v_mfma_f32_32x32x16_bf16 v[64:79], v[212:215], v[6:9], v[64:79]
	ds_read_b128 v[212:215], v0 offset:13856
	v_mfma_f32_32x32x16_bf16 v[32:47], v[216:219], v[6:9], v[32:47]
	v_cvt_pk_f32_fp8_e32 v[6:7], v204
	v_cvt_pk_f32_fp8_sdwa v[8:9], v204 src0_sel:WORD_1
	v_cvt_pk_bf16_f32 v6, v6, v7
	v_cvt_pk_bf16_f32 v7, v8, v9
	v_cvt_pk_bf16_f32 v8, v10, v11
	v_cvt_pk_bf16_f32 v9, v12, v13
	ds_read_b128 v[10:13], v0 offset:4640
	s_waitcnt lgkmcnt(2)
	v_mfma_f32_32x32x16_bf16 v[144:159], v[2:5], v[6:9], v[144:159]
	s_waitcnt lgkmcnt(0)
	v_mfma_f32_32x32x16_bf16 v[112:127], v[10:13], v[6:9], v[112:127]
	v_mfma_f32_32x32x16_bf16 v[128:143], v[208:211], v[6:9], v[128:143]
	v_mfma_f32_32x32x16_bf16 v[96:111], v[212:215], v[6:9], v[96:111]
	v_cvt_pk_f32_fp8_e32 v[6:7], v192
	v_cvt_pk_f32_fp8_sdwa v[8:9], v192 src0_sel:WORD_1
	v_cvt_pk_f32_fp8_sdwa v[192:193], v193 src0_sel:WORD_1
	v_cvt_pk_bf16_f32 v6, v6, v7
	v_cvt_pk_bf16_f32 v7, v8, v9
	v_cvt_pk_bf16_f32 v8, v14, v15
	v_cvt_pk_bf16_f32 v9, v192, v193
	v_cvt_pk_f32_fp8_e32 v[14:15], v195
	v_cvt_pk_f32_fp8_sdwa v[192:193], v195 src0_sel:WORD_1
	v_mfma_f32_32x32x16_bf16 v[80:95], v[2:5], v[6:9], v[80:95]
	ds_read_b128 v[2:5], v0 offset:48
	v_mfma_f32_32x32x16_bf16 v[48:63], v[10:13], v[6:9], v[48:63]
	v_cvt_pk_f32_fp8_e32 v[10:11], v207
	v_cvt_pk_f32_fp8_sdwa v[12:13], v207 src0_sel:WORD_1
	v_mfma_f32_32x32x16_bf16 v[64:79], v[208:211], v[6:9], v[64:79]
	ds_read_b128 v[208:211], v0 offset:13872
	v_mfma_f32_32x32x16_bf16 v[32:47], v[212:215], v[6:9], v[32:47]
	v_cvt_pk_f32_fp8_e32 v[6:7], v206
	v_cvt_pk_f32_fp8_sdwa v[8:9], v206 src0_sel:WORD_1
	ds_read_b128 v[204:207], v0 offset:9264
	v_cvt_pk_bf16_f32 v6, v6, v7
	v_cvt_pk_bf16_f32 v7, v8, v9
	v_cvt_pk_bf16_f32 v8, v10, v11
	v_cvt_pk_bf16_f32 v9, v12, v13
	ds_read_b128 v[10:13], v0 offset:4656
	s_waitcnt lgkmcnt(3)
	v_mfma_f32_32x32x16_bf16 v[144:159], v[2:5], v[6:9], v[144:159]
	s_waitcnt lgkmcnt(0)
	v_mfma_f32_32x32x16_bf16 v[112:127], v[10:13], v[6:9], v[112:127]
	v_mfma_f32_32x32x16_bf16 v[128:143], v[204:207], v[6:9], v[128:143]
	v_mfma_f32_32x32x16_bf16 v[96:111], v[208:211], v[6:9], v[96:111]
	v_cvt_pk_f32_fp8_e32 v[6:7], v194
	v_cvt_pk_f32_fp8_sdwa v[8:9], v194 src0_sel:WORD_1
	v_cvt_pk_bf16_f32 v6, v6, v7
	v_cvt_pk_bf16_f32 v7, v8, v9
	v_cvt_pk_bf16_f32 v8, v14, v15
	v_cvt_pk_bf16_f32 v9, v192, v193
	s_nop 1
	v_mfma_f32_32x32x16_bf16 v[80:95], v[2:5], v[6:9], v[80:95]
	v_mfma_f32_32x32x16_bf16 v[48:63], v[10:13], v[6:9], v[48:63]
	v_mfma_f32_32x32x16_bf16 v[64:79], v[204:207], v[6:9], v[64:79]
	v_mfma_f32_32x32x16_bf16 v[32:47], v[208:211], v[6:9], v[32:47]
.LBB0_1308:
	v_mov_b32_e32 v0, v241
	s_waitcnt vmcnt(7)
	v_cvt_pk_f32_fp8_e32 v[2:3], v196
	v_cvt_pk_f32_fp8_sdwa v[4:5], v196 src0_sel:WORD_1
	v_cvt_pk_f32_fp8_e32 v[10:11], v197
	v_cvt_pk_f32_fp8_sdwa v[12:13], v197 src0_sel:WORD_1
	global_load_dwordx4 v[192:195], v0, s[46:47] offset:16
	v_mov_b32_e32 v0, v242
	global_load_dwordx4 v[6:9], v0, s[46:47] offset:16
	v_add_u32_e32 v0, s90, v246
	v_cvt_pk_bf16_f32 v2, v2, v3
	v_cvt_pk_bf16_f32 v3, v4, v5
	v_cvt_pk_bf16_f32 v4, v10, v11
	v_cvt_pk_bf16_f32 v5, v12, v13
	ds_read_b128 v[10:13], v0
	v_cvt_pk_f32_fp8_sdwa v[14:15], v199 src0_sel:WORD_1
	s_waitcnt lgkmcnt(0)
	v_mfma_f32_32x32x16_bf16 v[16:31], v[10:13], v[2:5], v[16:31]
	v_cvt_pk_f32_fp8_e32 v[2:3], v198
	v_cvt_pk_f32_fp8_sdwa v[4:5], v198 src0_sel:WORD_1
	v_cvt_pk_f32_fp8_e32 v[12:13], v199
	s_add_i32 s2, s26, 1
	v_cvt_pk_bf16_f32 v10, v2, v3
	v_mov_b32_e32 v2, v243
	v_cvt_pk_bf16_f32 v11, v4, v5
	global_load_dwordx4 v[2:5], v2, s[46:47]
	ds_read_b128 v[196:199], v0 offset:16
	ds_read_b128 v[212:215], v0 offset:32
	v_cvt_pk_bf16_f32 v12, v12, v13
	v_cvt_pk_bf16_f32 v13, v14, v15
	s_waitcnt vmcnt(9)
	v_cvt_pk_f32_fp8_e32 v[14:15], v201
	s_cmp_lg_u32 s26, 2
	s_waitcnt lgkmcnt(1)
	v_mfma_f32_32x32x16_bf16 v[16:31], v[196:199], v[10:13], v[16:31]
	v_cvt_pk_f32_fp8_e32 v[10:11], v200
	v_cvt_pk_f32_fp8_sdwa v[12:13], v200 src0_sel:WORD_1
	v_cvt_pk_f32_fp8_sdwa v[196:197], v201 src0_sel:WORD_1
	v_cvt_pk_f32_fp8_sdwa v[200:201], v203 src0_sel:WORD_1
	v_cvt_pk_bf16_f32 v10, v10, v11
	v_cvt_pk_bf16_f32 v11, v12, v13
	v_cvt_pk_bf16_f32 v12, v14, v15
	v_cvt_pk_bf16_f32 v13, v196, v197
	s_cselect_b32 s2, s2, 0
	s_mul_i32 s25, s2, 0x4800
	s_waitcnt lgkmcnt(0)
	v_mfma_f32_32x32x16_bf16 v[16:31], v[212:215], v[10:13], v[16:31]
	v_cvt_pk_f32_fp8_e32 v[10:11], v202
	v_cvt_pk_f32_fp8_sdwa v[12:13], v202 src0_sel:WORD_1
	v_cvt_pk_f32_fp8_e32 v[14:15], v203
	v_cvt_pk_bf16_f32 v199, v200, v201
	v_cvt_pk_bf16_f32 v196, v10, v11
	v_mov_b32_e32 v10, v243
	ds_read_b128 v[200:203], v0 offset:48
	v_add_u32_e32 v0, s25, v244
	s_add_i32 s25, s39, 4
	s_cmp_lt_u32 s39, 60
	s_cselect_b32 s25, s25, 0
	s_lshr_b32 s26, s25, 4
	s_add_i32 s26, s26, s66
	s_and_b32 s26, s26, 3
	s_add_i32 s26, s26, s27
	s_lshl_b32 s25, s25, 16
	s_lshl_b32 s26, s26, 8
	s_and_b32 s25, s25, 0xe0000
	v_cvt_pk_bf16_f32 v198, v14, v15
	s_waitcnt vmcnt(12)
	v_cvt_pk_bf16_f32 v14, v176, v180
	v_cvt_pk_bf16_f32 v15, v184, v188
	s_or_b32 s25, s26, s25
	v_cvt_pk_bf16_f32 v197, v12, v13
	global_load_dwordx4 v[10:13], v10, s[46:47] offset:16
	s_and_b32 s98, s49, 0x380
	s_cmp_lt_u32 s39, 62
	s_cselect_b32 s98, s98, 0
	s_add_u32 s98, s98, s54
	s_addc_u32 s99, 0, s55
	global_load_dwordx4 v[220:223], v241, s[98:99]
	global_load_dwordx4 v[224:227], v242, s[98:99]
	s_waitcnt lgkmcnt(0)
	s_barrier
	ds_write2_b32 v0, v14, v15 offset1:8
	v_cvt_pk_bf16_f32 v14, v177, v181
	v_cvt_pk_bf16_f32 v15, v185, v189
	v_add_u32_e32 v176, 0x400, v0
	s_add_u32 s46, s67, s25
	ds_write2_b32 v176, v14, v15 offset0:32 offset1:40
	v_cvt_pk_bf16_f32 v14, v178, v182
	v_cvt_pk_bf16_f32 v15, v186, v190
	v_add_u32_e32 v176, 0x800, v0
	s_addc_u32 s47, s38, 0
	ds_write2_b32 v176, v14, v15 offset0:64 offset1:72
	v_cvt_pk_bf16_f32 v14, v179, v183
	v_cvt_pk_bf16_f32 v15, v187, v191
	v_add_u32_e32 v0, 0xc00, v0
	s_add_u32 s90, s46, 0x4000
	ds_write2_b32 v0, v14, v15 offset0:96 offset1:104
	s_addc_u32 s91, s47, 0
	v_mov_b32_e32 v0, v238
	global_load_dwordx4 v[176:179], v0, s[46:47] nt
	global_load_dwordx4 v[180:183], v0, s[46:47] offset:1024 nt
	global_load_dwordx4 v[184:187], v0, s[90:91] nt
	global_load_dwordx4 v[188:191], v0, s[90:91] offset:1024 nt
	v_mfma_f32_32x32x16_bf16 v[16:31], v[200:203], v[196:199], v[16:31]
	s_cmp_gt_u32 s39, 61
	s_cselect_b64 s[46:47], -1, 0
	s_and_b32 s25, s49, 0x380
	s_cmp_lt_u32 s39, 62
	s_cselect_b32 s25, s25, 0
	s_add_u32 s90, s25, s54
	s_addc_u32 s91, 0, s55
	s_and_b64 vcc, exec, s[42:43]
	s_cbranch_vccnz .LBB0_1310
	s_waitcnt vmcnt(14)
	v_cvt_pk_f32_fp8_sdwa v[202:203], v228 src0_sel:WORD_1
	v_cvt_pk_f32_fp8_e32 v[212:213], v229
	v_add_u32_e32 v0, s56, v240
	ds_read_b128 v[196:199], v0
	v_cvt_pk_bf16_f32 v201, v202, v203
	v_cvt_pk_bf16_f32 v202, v212, v213
	ds_read_b128 v[212:215], v0 offset:4608
	ds_read_b128 v[216:219], v0 offset:9216
	ds_read_b128 v[248:251], v0 offset:13824
	v_cvt_pk_f32_fp8_e32 v[14:15], v228
	v_cvt_pk_f32_fp8_sdwa v[208:209], v229 src0_sel:WORD_1
	v_cvt_pk_bf16_f32 v200, v14, v15
	v_cvt_pk_bf16_f32 v203, v208, v209
	s_waitcnt vmcnt(14)
	v_cvt_pk_f32_fp8_e32 v[14:15], v232
	v_cvt_pk_f32_fp8_e32 v[208:209], v233
	s_waitcnt lgkmcnt(3)
	v_mfma_f32_32x32x16_bf16 v[144:159], v[196:199], v[200:203], v[144:159]
	s_waitcnt lgkmcnt(2)
	v_mfma_f32_32x32x16_bf16 v[112:127], v[212:215], v[200:203], v[112:127]
	s_waitcnt lgkmcnt(1)
	v_mfma_f32_32x32x16_bf16 v[128:143], v[216:219], v[200:203], v[128:143]
	s_waitcnt lgkmcnt(0)
	v_mfma_f32_32x32x16_bf16 v[96:111], v[248:251], v[200:203], v[96:111]
	v_cvt_pk_f32_fp8_sdwa v[202:203], v232 src0_sel:WORD_1
	v_cvt_pk_f32_fp8_sdwa v[204:205], v233 src0_sel:WORD_1
	v_cvt_pk_bf16_f32 v200, v14, v15
	v_cvt_pk_f32_fp8_e32 v[14:15], v230
	v_cvt_pk_bf16_f32 v201, v202, v203
	v_cvt_pk_bf16_f32 v202, v208, v209
	v_cvt_pk_bf16_f32 v203, v204, v205
	v_cvt_pk_f32_fp8_sdwa v[208:209], v231 src0_sel:WORD_1
	v_cvt_pk_f32_fp8_e32 v[204:205], v231
	v_mfma_f32_32x32x16_bf16 v[80:95], v[196:199], v[200:203], v[80:95]
	ds_read_b128 v[196:199], v0 offset:16
	v_mfma_f32_32x32x16_bf16 v[48:63], v[212:215], v[200:203], v[48:63]
	ds_read_b128 v[212:215], v0 offset:9232
	v_mfma_f32_32x32x16_bf16 v[64:79], v[216:219], v[200:203], v[64:79]
	ds_read_b128 v[216:219], v0 offset:13840
	v_mfma_f32_32x32x16_bf16 v[32:47], v[248:251], v[200:203], v[32:47]
	v_cvt_pk_f32_fp8_sdwa v[202:203], v230 src0_sel:WORD_1
	v_cvt_pk_bf16_f32 v200, v14, v15
	v_cvt_pk_f32_fp8_e32 v[14:15], v234
	v_cvt_pk_bf16_f32 v201, v202, v203
	v_cvt_pk_bf16_f32 v203, v208, v209
	ds_read_b128 v[208:211], v0 offset:4624
	v_cvt_pk_bf16_f32 v202, v204, v205
	v_cvt_pk_f32_fp8_e32 v[204:205], v235
	s_waitcnt lgkmcnt(3)
	v_mfma_f32_32x32x16_bf16 v[144:159], v[196:199], v[200:203], v[144:159]
	s_waitcnt lgkmcnt(0)
	v_mfma_f32_32x32x16_bf16 v[112:127], v[208:211], v[200:203], v[112:127]
	v_mfma_f32_32x32x16_bf16 v[128:143], v[212:215], v[200:203], v[128:143]
	v_mfma_f32_32x32x16_bf16 v[96:111], v[216:219], v[200:203], v[96:111]
	v_cvt_pk_f32_fp8_sdwa v[202:203], v234 src0_sel:WORD_1
	v_cvt_pk_f32_fp8_sdwa v[206:207], v235 src0_sel:WORD_1
	v_cvt_pk_bf16_f32 v200, v14, v15
	s_waitcnt vmcnt(8)
	v_cvt_pk_f32_fp8_e32 v[14:15], v192
	v_cvt_pk_bf16_f32 v201, v202, v203
	v_cvt_pk_bf16_f32 v202, v204, v205
	v_cvt_pk_bf16_f32 v203, v206, v207
	v_cvt_pk_f32_fp8_e32 v[204:205], v193
	s_nop 0
	v_mfma_f32_32x32x16_bf16 v[80:95], v[196:199], v[200:203], v[80:95]
	ds_read_b128 v[196:199], v0 offset:32
	v_mfma_f32_32x32x16_bf16 v[48:63], v[208:211], v[200:203], v[48:63]
	ds_read_b128 v[208:211], v0 offset:9248
	v_mfma_f32_32x32x16_bf16 v[64:79], v[212:215], v[200:203], v[64:79]
	ds_read_b128 v[212:215], v0 offset:13856
	v_mfma_f32_32x32x16_bf16 v[32:47], v[216:219], v[200:203], v[32:47]
	v_cvt_pk_f32_fp8_sdwa v[202:203], v192 src0_sel:WORD_1
	v_cvt_pk_f32_fp8_sdwa v[192:193], v193 src0_sel:WORD_1
	v_cvt_pk_bf16_f32 v200, v14, v15
	v_cvt_pk_f32_fp8_e32 v[14:15], v6
	v_cvt_pk_bf16_f32 v201, v202, v203
	v_cvt_pk_bf16_f32 v202, v204, v205
	ds_read_b128 v[204:207], v0 offset:4640
	v_cvt_pk_bf16_f32 v203, v192, v193
	v_cvt_pk_f32_fp8_sdwa v[192:193], v6 src0_sel:WORD_1
	s_waitcnt lgkmcnt(3)
	v_mfma_f32_32x32x16_bf16 v[144:159], v[196:199], v[200:203], v[144:159]
	s_waitcnt lgkmcnt(0)
	v_mfma_f32_32x32x16_bf16 v[112:127], v[204:207], v[200:203], v[112:127]
	v_mfma_f32_32x32x16_bf16 v[128:143], v[208:211], v[200:203], v[128:143]
	v_mfma_f32_32x32x16_bf16 v[96:111], v[212:215], v[200:203], v[96:111]
	v_cvt_pk_f32_fp8_e32 v[202:203], v7
	v_cvt_pk_f32_fp8_sdwa v[6:7], v7 src0_sel:WORD_1
	v_cvt_pk_bf16_f32 v200, v14, v15
	v_cvt_pk_bf16_f32 v201, v192, v193
	v_cvt_pk_bf16_f32 v202, v202, v203
	v_cvt_pk_bf16_f32 v203, v6, v7
	v_cvt_pk_f32_fp8_e32 v[6:7], v194
	v_cvt_pk_f32_fp8_sdwa v[14:15], v194 src0_sel:WORD_1
	v_mfma_f32_32x32x16_bf16 v[80:95], v[196:199], v[200:203], v[80:95]
	ds_read_b128 v[196:199], v0 offset:48
	v_cvt_pk_bf16_f32 v192, v6, v7
	v_cvt_pk_bf16_f32 v193, v14, v15
	v_cvt_pk_f32_fp8_e32 v[6:7], v8
	v_cvt_pk_f32_fp8_sdwa v[14:15], v8 src0_sel:WORD_1
	v_cvt_pk_bf16_f32 v6, v6, v7
	v_mfma_f32_32x32x16_bf16 v[48:63], v[204:207], v[200:203], v[48:63]
	ds_read_b128 v[204:207], v0 offset:9264
	v_cvt_pk_bf16_f32 v7, v14, v15
	v_mfma_f32_32x32x16_bf16 v[64:79], v[208:211], v[200:203], v[64:79]
	ds_read_b128 v[208:211], v0 offset:13872
	v_mfma_f32_32x32x16_bf16 v[32:47], v[212:215], v[200:203], v[32:47]
	v_cvt_pk_f32_fp8_e32 v[200:201], v195
	v_cvt_pk_f32_fp8_sdwa v[202:203], v195 src0_sel:WORD_1
	v_cvt_pk_bf16_f32 v194, v200, v201
	v_cvt_pk_bf16_f32 v195, v202, v203
	ds_read_b128 v[200:203], v0 offset:4656
	s_waitcnt lgkmcnt(3)
	v_mfma_f32_32x32x16_bf16 v[144:159], v[196:199], v[192:195], v[144:159]
	s_waitcnt lgkmcnt(0)
	v_mfma_f32_32x32x16_bf16 v[112:127], v[200:203], v[192:195], v[112:127]
	v_mfma_f32_32x32x16_bf16 v[128:143], v[204:207], v[192:195], v[128:143]
	v_mfma_f32_32x32x16_bf16 v[96:111], v[208:211], v[192:195], v[96:111]
	v_cvt_pk_f32_fp8_e32 v[192:193], v9
	v_cvt_pk_f32_fp8_sdwa v[194:195], v9 src0_sel:WORD_1
	v_cvt_pk_bf16_f32 v8, v192, v193
	v_cvt_pk_bf16_f32 v9, v194, v195
	s_nop 1
	v_mfma_f32_32x32x16_bf16 v[80:95], v[196:199], v[6:9], v[80:95]
	v_mfma_f32_32x32x16_bf16 v[48:63], v[200:203], v[6:9], v[48:63]
	v_mfma_f32_32x32x16_bf16 v[64:79], v[204:207], v[6:9], v[64:79]
	v_mfma_f32_32x32x16_bf16 v[32:47], v[208:211], v[6:9], v[32:47]
.LBB0_1310:
	v_mov_b32_e32 v0, v241
	global_load_dwordx4 v[204:207], v0, s[90:91] offset:16
	v_mov_b32_e32 v0, v242
	s_add_i32 s25, s33, s56
	global_load_dwordx4 v[192:195], v0, s[90:91] offset:16
	v_add_u32_e32 v0, s25, v240
	ds_read_b128 v[196:199], v0
	s_waitcnt vmcnt(9)
	v_cvt_pk_f32_fp8_e32 v[6:7], v2
	v_cvt_pk_f32_fp8_sdwa v[8:9], v2 src0_sel:WORD_1
	v_cvt_pk_f32_fp8_e32 v[14:15], v3
	v_cvt_pk_f32_fp8_sdwa v[2:3], v3 src0_sel:WORD_1
	v_cvt_pk_bf16_f32 v6, v6, v7
	v_cvt_pk_bf16_f32 v7, v8, v9
	v_cvt_pk_bf16_f32 v8, v14, v15
	v_cvt_pk_bf16_f32 v9, v2, v3
	v_cvt_pk_f32_fp8_e32 v[2:3], v4
	v_cvt_pk_f32_fp8_sdwa v[14:15], v5 src0_sel:WORD_1
	s_waitcnt lgkmcnt(0)
	v_mfma_f32_32x32x16_bf16 v[16:31], v[196:199], v[6:9], v[16:31]
	v_cvt_pk_f32_fp8_sdwa v[6:7], v4 src0_sel:WORD_1
	v_cvt_pk_f32_fp8_e32 v[8:9], v5
	v_cvt_pk_bf16_f32 v2, v2, v3
	v_cvt_pk_bf16_f32 v5, v14, v15
	v_cvt_pk_bf16_f32 v3, v6, v7
	v_mov_b32_e32 v6, v243
	v_cvt_pk_bf16_f32 v4, v8, v9
	global_load_dwordx4 v[196:199], v6, s[90:91]
	ds_read_b128 v[6:9], v0 offset:16
	ds_read_b128 v[200:203], v0 offset:32
	s_waitcnt lgkmcnt(1)
	v_mfma_f32_32x32x16_bf16 v[16:31], v[6:9], v[2:5], v[16:31]
	s_waitcnt vmcnt(9)
	v_cvt_pk_f32_fp8_e32 v[2:3], v10
	v_cvt_pk_f32_fp8_sdwa v[4:5], v10 src0_sel:WORD_1
	v_cvt_pk_f32_fp8_e32 v[6:7], v11
	v_cvt_pk_f32_fp8_sdwa v[8:9], v11 src0_sel:WORD_1
	v_cvt_pk_bf16_f32 v2, v2, v3
	v_cvt_pk_bf16_f32 v3, v4, v5
	v_cvt_pk_bf16_f32 v4, v6, v7
	v_cvt_pk_bf16_f32 v5, v8, v9
	v_cvt_pk_f32_fp8_e32 v[6:7], v13
	v_cvt_pk_f32_fp8_sdwa v[8:9], v13 src0_sel:WORD_1
	s_waitcnt lgkmcnt(0)
	v_mfma_f32_32x32x16_bf16 v[16:31], v[200:203], v[2:5], v[16:31]
	v_cvt_pk_f32_fp8_e32 v[2:3], v12
	v_cvt_pk_f32_fp8_sdwa v[4:5], v12 src0_sel:WORD_1
	s_and_b32 s26, s39, 14
	s_cmp_lg_u32 s26, 14
	v_cvt_pk_bf16_f32 v2, v2, v3
	v_cvt_pk_bf16_f32 v3, v4, v5
	v_cvt_pk_bf16_f32 v4, v6, v7
	v_mov_b32_e32 v6, v243
	global_load_dwordx4 v[200:203], v6, s[90:91] offset:16
	v_cvt_pk_bf16_f32 v5, v8, v9
	ds_read_b128 v[6:9], v0 offset:48
	s_waitcnt lgkmcnt(0)
	v_mfma_f32_32x32x16_bf16 v[16:31], v[6:9], v[2:5], v[16:31]
	s_cbranch_scc1 .LBB0_1305
	s_lshr_b32 s25, s39, 4
	s_add_i32 s25, s25, s66
	v_mbcnt_lo_u32_b32 v248, -1, 0
	v_mbcnt_hi_u32_b32 v248, -1, v248
	s_and_b32 s56, s25, 3
	v_ashrrev_i32_e32 v0, 5, v248
	v_lshlrev_b32_e32 v218, 4, v0
	s_add_i32 s56, s56, s27
	v_and_b32_e32 v247, 31, v248
	s_and_b64 vcc, exec, s[42:43]
	v_ashrrev_i32_e32 v219, 31, v218
	s_cbranch_vccnz .LBB0_1315
	v_lshl_add_u32 v6, v247, 2, s87
	ds_read_b32 v0, v6 offset:55296
	s_lshl_b32 s25, s56, 6
	s_add_u32 s42, s58, s25
	s_addc_u32 s43, s59, 0
	v_lshl_add_u64 v[2:3], s[42:43], 0, v[218:219]
	s_waitcnt lgkmcnt(0)
	v_lshlrev_b64 v[4:5], 8, v[0:1]
	v_mul_f32_e32 v0, 0xbfb8aa3b, v144
	v_exp_f32_e32 v0, v0
	v_lshl_add_u64 v[4:5], v[2:3], 0, v[4:5]
	v_add_f32_e32 v0, 1.0, v0
	v_div_scale_f32 v7, s[42:43], v0, v0, v144
	v_rcp_f32_e32 v8, v7
	s_nop 0
	v_fma_f32 v9, -v7, v8, 1.0
	v_fmac_f32_e32 v8, v9, v8
	v_div_scale_f32 v9, vcc, v144, v0, v144
	v_mul_f32_e32 v10, v9, v8
	v_fma_f32 v11, -v7, v10, v9
	v_fmac_f32_e32 v10, v11, v8
	v_fma_f32 v7, -v7, v10, v9
	v_div_fmas_f32 v7, v7, v8, v10
	v_div_fixup_f32 v0, v7, v0, v144
	v_mul_f32_e32 v7, 0xbfb8aa3b, v148
	v_exp_f32_e32 v7, v7
	v_mul_f32_e32 v0, v128, v0
	v_add_f32_e32 v7, 1.0, v7
	v_div_scale_f32 v8, s[42:43], v7, v7, v148
	v_rcp_f32_e32 v9, v8
	s_nop 0
	v_fma_f32 v10, -v8, v9, 1.0
	v_fmac_f32_e32 v9, v10, v9
	v_div_scale_f32 v10, vcc, v148, v7, v148
	v_mul_f32_e32 v11, v10, v9
	v_fma_f32 v12, -v8, v11, v10
	v_fmac_f32_e32 v11, v12, v9
	v_fma_f32 v8, -v8, v11, v10
	v_div_fmas_f32 v8, v8, v9, v11
	v_div_fixup_f32 v7, v8, v7, v148
	v_mul_f32_e32 v8, 0xbfb8aa3b, v152
	v_exp_f32_e32 v8, v8
	v_mul_f32_e32 v7, v132, v7
	v_add_f32_e32 v8, 1.0, v8
	v_div_scale_f32 v9, s[42:43], v8, v8, v152
	v_rcp_f32_e32 v10, v9
	s_nop 0
	v_fma_f32 v11, -v9, v10, 1.0
	v_fmac_f32_e32 v10, v11, v10
	v_div_scale_f32 v11, vcc, v152, v8, v152
	v_mul_f32_e32 v12, v11, v10
	v_fma_f32 v13, -v9, v12, v11
	v_fmac_f32_e32 v12, v13, v10
	v_fma_f32 v9, -v9, v12, v11
	v_div_fmas_f32 v9, v9, v10, v12
	v_div_fixup_f32 v8, v9, v8, v152
	v_mul_f32_e32 v9, 0xbfb8aa3b, v156
	v_exp_f32_e32 v9, v9
	v_mul_f32_e32 v8, v136, v8
	v_add_f32_e32 v9, 1.0, v9
	v_div_scale_f32 v10, s[42:43], v9, v9, v156
	v_rcp_f32_e32 v11, v10
	s_nop 0
	v_fma_f32 v12, -v10, v11, 1.0
	v_fmac_f32_e32 v11, v12, v11
	v_div_scale_f32 v12, vcc, v156, v9, v156
	v_mul_f32_e32 v13, v12, v11
	v_fma_f32 v14, -v10, v13, v12
	v_fmac_f32_e32 v13, v14, v11
	v_fma_f32 v10, -v10, v13, v12
	v_div_fmas_f32 v10, v10, v11, v13
	v_div_fixup_f32 v9, v10, v9, v156
	v_mul_f32_e32 v10, 0xbfb8aa3b, v145
	v_exp_f32_e32 v10, v10
	v_mul_f32_e32 v9, v140, v9
	v_add_f32_e32 v10, 1.0, v10
	v_div_scale_f32 v11, s[42:43], v10, v10, v145
	v_rcp_f32_e32 v12, v11
	s_nop 0
	v_fma_f32 v13, -v11, v12, 1.0
	v_fmac_f32_e32 v12, v13, v12
	v_div_scale_f32 v13, vcc, v145, v10, v145
	v_mul_f32_e32 v14, v13, v12
	v_fma_f32 v15, -v11, v14, v13
	v_fmac_f32_e32 v14, v15, v12
	v_fma_f32 v11, -v11, v14, v13
	v_div_fmas_f32 v11, v11, v12, v14
	v_div_fixup_f32 v10, v11, v10, v145
	v_mul_f32_e32 v11, 0xbfb8aa3b, v149
	v_exp_f32_e32 v11, v11
	v_mul_f32_e32 v10, v129, v10
	v_add_f32_e32 v11, 1.0, v11
	v_div_scale_f32 v12, s[42:43], v11, v11, v149
	v_rcp_f32_e32 v13, v12
	s_nop 0
	v_fma_f32 v14, -v12, v13, 1.0
	v_fmac_f32_e32 v13, v14, v13
	v_div_scale_f32 v14, vcc, v149, v11, v149
	v_mul_f32_e32 v15, v14, v13
	v_fma_f32 v128, -v12, v15, v14
	v_fmac_f32_e32 v15, v128, v13
	v_fma_f32 v12, -v12, v15, v14
	v_div_fmas_f32 v12, v12, v13, v15
	v_div_fixup_f32 v11, v12, v11, v149
	v_mul_f32_e32 v12, 0xbfb8aa3b, v153
	v_exp_f32_e32 v12, v12
	v_mul_f32_e32 v11, v133, v11
	v_add_f32_e32 v12, 1.0, v12
	v_div_scale_f32 v13, s[42:43], v12, v12, v153
	v_rcp_f32_e32 v14, v13
	s_nop 0
	v_fma_f32 v15, -v13, v14, 1.0
	v_fmac_f32_e32 v14, v15, v14
	v_div_scale_f32 v15, vcc, v153, v12, v153
	v_mul_f32_e32 v128, v15, v14
	v_fma_f32 v129, -v13, v128, v15
	v_fmac_f32_e32 v128, v129, v14
	v_fma_f32 v13, -v13, v128, v15
	v_div_fmas_f32 v13, v13, v14, v128
	v_div_fixup_f32 v12, v13, v12, v153
	v_mul_f32_e32 v13, 0xbfb8aa3b, v157
	v_exp_f32_e32 v13, v13
	v_mul_f32_e32 v12, v137, v12
	v_add_f32_e32 v13, 1.0, v13
	v_div_scale_f32 v14, s[42:43], v13, v13, v157
	v_rcp_f32_e32 v15, v14
	s_nop 0
	v_fma_f32 v128, -v14, v15, 1.0
	v_fmac_f32_e32 v15, v128, v15
	v_div_scale_f32 v128, vcc, v157, v13, v157
	v_mul_f32_e32 v129, v128, v15
	v_fma_f32 v132, -v14, v129, v128
	v_fmac_f32_e32 v129, v132, v15
	v_fma_f32 v14, -v14, v129, v128
	v_div_fmas_f32 v14, v14, v15, v129
	v_div_fixup_f32 v13, v14, v13, v157
	v_mul_f32_e32 v14, 0xbfb8aa3b, v146
	v_exp_f32_e32 v14, v14
	v_mul_f32_e32 v13, v141, v13
	v_add_f32_e32 v14, 1.0, v14
	v_div_scale_f32 v15, s[42:43], v14, v14, v146
	v_rcp_f32_e32 v128, v15
	s_nop 0
	v_fma_f32 v129, -v15, v128, 1.0
	v_fmac_f32_e32 v128, v129, v128
	v_div_scale_f32 v129, vcc, v146, v14, v146
	v_mul_f32_e32 v132, v129, v128
	v_fma_f32 v133, -v15, v132, v129
	v_fmac_f32_e32 v132, v133, v128
	v_fma_f32 v15, -v15, v132, v129
	v_div_fmas_f32 v15, v15, v128, v132
	v_div_fixup_f32 v14, v15, v14, v146
	v_mul_f32_e32 v15, 0xbfb8aa3b, v150
	v_exp_f32_e32 v15, v15
	v_mul_f32_e32 v14, v130, v14
	v_add_f32_e32 v15, 1.0, v15
	v_div_scale_f32 v128, s[42:43], v15, v15, v150
	v_rcp_f32_e32 v129, v128
	s_nop 0
	v_fma_f32 v130, -v128, v129, 1.0
	v_fmac_f32_e32 v129, v130, v129
	v_div_scale_f32 v130, vcc, v150, v15, v150
	v_mul_f32_e32 v132, v130, v129
	v_fma_f32 v133, -v128, v132, v130
	v_fmac_f32_e32 v132, v133, v129
	v_fma_f32 v128, -v128, v132, v130
	v_div_fmas_f32 v128, v128, v129, v132
	v_div_fixup_f32 v15, v128, v15, v150
	v_mul_f32_e32 v128, 0xbfb8aa3b, v154
	v_exp_f32_e32 v128, v128
	v_mul_f32_e32 v15, v134, v15
	v_add_f32_e32 v128, 1.0, v128
	v_div_scale_f32 v129, s[42:43], v128, v128, v154
	v_rcp_f32_e32 v130, v129
	s_nop 0
	v_fma_f32 v132, -v129, v130, 1.0
	v_fmac_f32_e32 v130, v132, v130
	v_div_scale_f32 v132, vcc, v154, v128, v154
	v_mul_f32_e32 v133, v132, v130
	v_fma_f32 v134, -v129, v133, v132
	v_fmac_f32_e32 v133, v134, v130
	v_fma_f32 v129, -v129, v133, v132
	v_div_fmas_f32 v129, v129, v130, v133
	v_div_fixup_f32 v128, v129, v128, v154
	v_mul_f32_e32 v132, v138, v128
	v_mul_f32_e32 v128, 0xbfb8aa3b, v158
	v_exp_f32_e32 v128, v128
	s_nop 0
	v_add_f32_e32 v128, 1.0, v128
	v_div_scale_f32 v129, s[42:43], v128, v128, v158
	v_rcp_f32_e32 v130, v129
	s_nop 0
	v_fma_f32 v133, -v129, v130, 1.0
	v_fmac_f32_e32 v130, v133, v130
	v_div_scale_f32 v133, vcc, v158, v128, v158
	v_mul_f32_e32 v134, v133, v130
	v_fma_f32 v136, -v129, v134, v133
	v_fmac_f32_e32 v134, v136, v130
	v_fma_f32 v129, -v129, v134, v133
	v_div_fmas_f32 v129, v129, v130, v134
	v_div_fixup_f32 v128, v129, v128, v158
	v_mul_f32_e32 v133, v142, v128
	v_mul_f32_e32 v128, 0xbfb8aa3b, v147
	v_exp_f32_e32 v128, v128
	s_nop 0
	v_add_f32_e32 v128, 1.0, v128
	v_div_scale_f32 v129, s[42:43], v128, v128, v147
	v_rcp_f32_e32 v130, v129
	s_nop 0
	v_fma_f32 v134, -v129, v130, 1.0
	v_fmac_f32_e32 v130, v134, v130
	v_div_scale_f32 v134, vcc, v147, v128, v147
	v_mul_f32_e32 v136, v134, v130
	v_fma_f32 v137, -v129, v136, v134
	v_fmac_f32_e32 v136, v137, v130
	v_fma_f32 v129, -v129, v136, v134
	v_div_fmas_f32 v129, v129, v130, v136
	v_div_fixup_f32 v128, v129, v128, v147
	v_mul_f32_e32 v134, v131, v128
	v_mul_f32_e32 v128, 0xbfb8aa3b, v151
	v_exp_f32_e32 v128, v128
	s_nop 0
	v_add_f32_e32 v128, 1.0, v128
	v_div_scale_f32 v129, s[42:43], v128, v128, v151
	v_rcp_f32_e32 v130, v129
	s_nop 0
	v_fma_f32 v131, -v129, v130, 1.0
	v_fmac_f32_e32 v130, v131, v130
	v_div_scale_f32 v131, vcc, v151, v128, v151
	v_mul_f32_e32 v136, v131, v130
	v_fma_f32 v137, -v129, v136, v131
	v_fmac_f32_e32 v136, v137, v130
	v_fma_f32 v129, -v129, v136, v131
	v_div_fmas_f32 v129, v129, v130, v136
	v_div_fixup_f32 v128, v129, v128, v151
	v_mul_f32_e32 v135, v135, v128
	v_mul_f32_e32 v128, 0xbfb8aa3b, v155
	v_exp_f32_e32 v128, v128
	s_nop 0
	v_add_f32_e32 v128, 1.0, v128
	v_div_scale_f32 v129, s[42:43], v128, v128, v155
	v_rcp_f32_e32 v130, v129
	s_nop 0
	v_fma_f32 v131, -v129, v130, 1.0
	v_fmac_f32_e32 v130, v131, v130
	v_div_scale_f32 v131, vcc, v155, v128, v155
	v_mul_f32_e32 v136, v131, v130
	v_fma_f32 v137, -v129, v136, v131
	v_fmac_f32_e32 v136, v137, v130
	v_fma_f32 v129, -v129, v136, v131
	v_div_fmas_f32 v129, v129, v130, v136
	v_div_fixup_f32 v128, v129, v128, v155
	v_mul_f32_e32 v136, v139, v128
	v_mul_f32_e32 v128, 0xbfb8aa3b, v159
	v_exp_f32_e32 v128, v128
	s_nop 0
	v_add_f32_e32 v128, 1.0, v128
	v_div_scale_f32 v129, s[42:43], v128, v128, v159
	v_rcp_f32_e32 v130, v129
	s_nop 0
	v_fma_f32 v131, -v129, v130, 1.0
	v_fmac_f32_e32 v130, v131, v130
	v_div_scale_f32 v131, vcc, v159, v128, v159
	v_mul_f32_e32 v137, v131, v130
	v_fma_f32 v138, -v129, v137, v131
	v_fmac_f32_e32 v137, v138, v130
	v_fma_f32 v129, -v129, v137, v131
	v_div_fmas_f32 v129, v129, v130, v137
	v_div_fixup_f32 v128, v129, v128, v159
	v_mul_f32_e32 v137, v143, v128
	v_mov_b32_e32 v128, v1
	v_cvt_pk_fp8_f32 v128, v0, v7
	v_mul_f32_e32 v0, 0xbfb8aa3b, v112
	v_exp_f32_e32 v0, v0
	v_mov_b32_e32 v129, v1
	v_cvt_pk_fp8_f32 v128, v8, v9 op_sel:[0,0,1]
	v_cvt_pk_fp8_f32 v129, v10, v11
	v_add_f32_e32 v0, 1.0, v0
	v_div_scale_f32 v7, s[42:43], v0, v0, v112
	v_rcp_f32_e32 v8, v7
	v_cvt_pk_fp8_f32 v129, v12, v13 op_sel:[0,0,1]
	v_mov_b32_e32 v130, v1
	v_cvt_pk_fp8_f32 v130, v14, v15
	v_fma_f32 v9, -v7, v8, 1.0
	v_fmac_f32_e32 v8, v9, v8
	v_div_scale_f32 v9, vcc, v112, v0, v112
	v_mul_f32_e32 v10, v9, v8
	v_fma_f32 v11, -v7, v10, v9
	v_fmac_f32_e32 v10, v11, v8
	v_fma_f32 v7, -v7, v10, v9
	v_div_fmas_f32 v7, v7, v8, v10
	v_div_fixup_f32 v0, v7, v0, v112
	v_mul_f32_e32 v7, 0xbfb8aa3b, v116
	v_exp_f32_e32 v7, v7
	v_mul_f32_e32 v0, v96, v0
	v_mov_b32_e32 v131, v1
	v_cvt_pk_fp8_f32 v131, v134, v135
	v_add_f32_e32 v7, 1.0, v7
	v_div_scale_f32 v8, s[42:43], v7, v7, v116
	v_rcp_f32_e32 v9, v8
	v_cvt_pk_fp8_f32 v130, v132, v133 op_sel:[0,0,1]
	v_cvt_pk_fp8_f32 v131, v136, v137 op_sel:[0,0,1]
	v_fma_f32 v10, -v8, v9, 1.0
	v_fmac_f32_e32 v9, v10, v9
	v_div_scale_f32 v10, vcc, v116, v7, v116
	v_mul_f32_e32 v11, v10, v9
	v_fma_f32 v12, -v8, v11, v10
	v_fmac_f32_e32 v11, v12, v9
	v_fma_f32 v8, -v8, v11, v10
	v_div_fmas_f32 v8, v8, v9, v11
	v_div_fixup_f32 v7, v8, v7, v116
	v_mul_f32_e32 v8, 0xbfb8aa3b, v120
	v_exp_f32_e32 v8, v8
	v_mul_f32_e32 v7, v100, v7
	global_store_dwordx4 v[4:5], v[128:131], off
	v_add_f32_e32 v8, 1.0, v8
	v_div_scale_f32 v9, s[42:43], v8, v8, v120
	v_rcp_f32_e32 v10, v9
	s_nop 0
	v_fma_f32 v11, -v9, v10, 1.0
	v_fmac_f32_e32 v10, v11, v10
	v_div_scale_f32 v11, vcc, v120, v8, v120
	v_mul_f32_e32 v12, v11, v10
	v_fma_f32 v13, -v9, v12, v11
	v_fmac_f32_e32 v12, v13, v10
	v_fma_f32 v9, -v9, v12, v11
	v_div_fmas_f32 v9, v9, v10, v12
	v_div_fixup_f32 v8, v9, v8, v120
	v_mul_f32_e32 v9, 0xbfb8aa3b, v124
	v_exp_f32_e32 v9, v9
	v_mul_f32_e32 v8, v104, v8
	v_add_f32_e32 v9, 1.0, v9
	v_div_scale_f32 v10, s[42:43], v9, v9, v124
	v_rcp_f32_e32 v11, v10
	s_nop 0
	v_fma_f32 v12, -v10, v11, 1.0
	v_fmac_f32_e32 v11, v12, v11
	v_div_scale_f32 v12, vcc, v124, v9, v124
	v_mul_f32_e32 v13, v12, v11
	v_fma_f32 v14, -v10, v13, v12
	v_fmac_f32_e32 v13, v14, v11
	v_fma_f32 v10, -v10, v13, v12
	v_div_fmas_f32 v10, v10, v11, v13
	v_div_fixup_f32 v9, v10, v9, v124
	v_mul_f32_e32 v10, 0xbfb8aa3b, v113
	v_exp_f32_e32 v10, v10
	v_mul_f32_e32 v9, v108, v9
	v_add_f32_e32 v10, 1.0, v10
	v_div_scale_f32 v11, s[42:43], v10, v10, v113
	v_rcp_f32_e32 v12, v11
	s_nop 0
	v_fma_f32 v13, -v11, v12, 1.0
	v_fmac_f32_e32 v12, v13, v12
	v_div_scale_f32 v13, vcc, v113, v10, v113
	v_mul_f32_e32 v14, v13, v12
	v_fma_f32 v15, -v11, v14, v13
	v_fmac_f32_e32 v14, v15, v12
	v_fma_f32 v11, -v11, v14, v13
	v_div_fmas_f32 v11, v11, v12, v14
	v_div_fixup_f32 v10, v11, v10, v113
	v_mul_f32_e32 v11, 0xbfb8aa3b, v117
	v_exp_f32_e32 v11, v11
	v_mul_f32_e32 v10, v97, v10
	v_add_f32_e32 v11, 1.0, v11
	v_div_scale_f32 v12, s[42:43], v11, v11, v117
	v_rcp_f32_e32 v13, v12
	s_nop 0
	v_fma_f32 v14, -v12, v13, 1.0
	v_fmac_f32_e32 v13, v14, v13
	v_div_scale_f32 v14, vcc, v117, v11, v117
	v_mul_f32_e32 v15, v14, v13
	v_fma_f32 v96, -v12, v15, v14
	v_fmac_f32_e32 v15, v96, v13
	v_fma_f32 v12, -v12, v15, v14
	v_div_fmas_f32 v12, v12, v13, v15
	v_div_fixup_f32 v11, v12, v11, v117
	v_mul_f32_e32 v12, 0xbfb8aa3b, v121
	v_exp_f32_e32 v12, v12
	v_mul_f32_e32 v11, v101, v11
	v_add_f32_e32 v12, 1.0, v12
	v_div_scale_f32 v13, s[42:43], v12, v12, v121
	v_rcp_f32_e32 v14, v13
	s_nop 0
	v_fma_f32 v15, -v13, v14, 1.0
	v_fmac_f32_e32 v14, v15, v14
	v_div_scale_f32 v15, vcc, v121, v12, v121
	v_mul_f32_e32 v96, v15, v14
	v_fma_f32 v97, -v13, v96, v15
	v_fmac_f32_e32 v96, v97, v14
	v_fma_f32 v13, -v13, v96, v15
	v_div_fmas_f32 v13, v13, v14, v96
	v_div_fixup_f32 v12, v13, v12, v121
	v_mul_f32_e32 v13, 0xbfb8aa3b, v125
	v_exp_f32_e32 v13, v13
	v_mul_f32_e32 v12, v105, v12
	v_add_f32_e32 v13, 1.0, v13
	v_div_scale_f32 v14, s[42:43], v13, v13, v125
	v_rcp_f32_e32 v15, v14
	s_nop 0
	v_fma_f32 v96, -v14, v15, 1.0
	v_fmac_f32_e32 v15, v96, v15
	v_div_scale_f32 v96, vcc, v125, v13, v125
	v_mul_f32_e32 v97, v96, v15
	v_fma_f32 v100, -v14, v97, v96
	v_fmac_f32_e32 v97, v100, v15
	v_fma_f32 v14, -v14, v97, v96
	v_div_fmas_f32 v14, v14, v15, v97
	v_div_fixup_f32 v13, v14, v13, v125
	v_mul_f32_e32 v14, 0xbfb8aa3b, v114
	v_exp_f32_e32 v14, v14
	v_mul_f32_e32 v13, v109, v13
	v_add_f32_e32 v14, 1.0, v14
	v_div_scale_f32 v15, s[42:43], v14, v14, v114
	v_rcp_f32_e32 v96, v15
	s_nop 0
	v_fma_f32 v97, -v15, v96, 1.0
	v_fmac_f32_e32 v96, v97, v96
	v_div_scale_f32 v97, vcc, v114, v14, v114
	v_mul_f32_e32 v100, v97, v96
	v_fma_f32 v101, -v15, v100, v97
	v_fmac_f32_e32 v100, v101, v96
	v_fma_f32 v15, -v15, v100, v97
	v_div_fmas_f32 v15, v15, v96, v100
	v_div_fixup_f32 v14, v15, v14, v114
	v_mul_f32_e32 v15, 0xbfb8aa3b, v118
	v_exp_f32_e32 v15, v15
	v_mul_f32_e32 v14, v98, v14
	v_add_f32_e32 v15, 1.0, v15
	v_div_scale_f32 v96, s[42:43], v15, v15, v118
	v_rcp_f32_e32 v97, v96
	s_nop 0
	v_fma_f32 v98, -v96, v97, 1.0
	v_fmac_f32_e32 v97, v98, v97
	v_div_scale_f32 v98, vcc, v118, v15, v118
	v_mul_f32_e32 v100, v98, v97
	v_fma_f32 v101, -v96, v100, v98
	v_fmac_f32_e32 v100, v101, v97
	v_fma_f32 v96, -v96, v100, v98
	v_div_fmas_f32 v96, v96, v97, v100
	v_div_fixup_f32 v15, v96, v15, v118
	v_mul_f32_e32 v96, 0xbfb8aa3b, v122
	v_exp_f32_e32 v96, v96
	v_mul_f32_e32 v15, v102, v15
	v_add_f32_e32 v96, 1.0, v96
	v_div_scale_f32 v97, s[42:43], v96, v96, v122
	v_rcp_f32_e32 v98, v97
	s_nop 0
	v_fma_f32 v100, -v97, v98, 1.0
	v_fmac_f32_e32 v98, v100, v98
	v_div_scale_f32 v100, vcc, v122, v96, v122
	v_mul_f32_e32 v101, v100, v98
	v_fma_f32 v102, -v97, v101, v100
	v_fmac_f32_e32 v101, v102, v98
	v_fma_f32 v97, -v97, v101, v100
	v_div_fmas_f32 v97, v97, v98, v101
	v_div_fixup_f32 v96, v97, v96, v122
	v_mul_f32_e32 v100, v106, v96
	v_mul_f32_e32 v96, 0xbfb8aa3b, v126
	v_exp_f32_e32 v96, v96
	s_nop 0
	v_add_f32_e32 v96, 1.0, v96
	v_div_scale_f32 v97, s[42:43], v96, v96, v126
	v_rcp_f32_e32 v98, v97
	s_nop 0
	v_fma_f32 v101, -v97, v98, 1.0
	v_fmac_f32_e32 v98, v101, v98
	v_div_scale_f32 v101, vcc, v126, v96, v126
	v_mul_f32_e32 v102, v101, v98
	v_fma_f32 v104, -v97, v102, v101
	v_fmac_f32_e32 v102, v104, v98
	v_fma_f32 v97, -v97, v102, v101
	v_div_fmas_f32 v97, v97, v98, v102
	v_div_fixup_f32 v96, v97, v96, v126
	v_mul_f32_e32 v101, v110, v96
	v_mul_f32_e32 v96, 0xbfb8aa3b, v115
	v_exp_f32_e32 v96, v96
	s_nop 0
	v_add_f32_e32 v96, 1.0, v96
	v_div_scale_f32 v97, s[42:43], v96, v96, v115
	v_rcp_f32_e32 v98, v97
	s_nop 0
	v_fma_f32 v102, -v97, v98, 1.0
	v_fmac_f32_e32 v98, v102, v98
	v_div_scale_f32 v102, vcc, v115, v96, v115
	v_mul_f32_e32 v104, v102, v98
	v_fma_f32 v105, -v97, v104, v102
	v_fmac_f32_e32 v104, v105, v98
	v_fma_f32 v97, -v97, v104, v102
	v_div_fmas_f32 v97, v97, v98, v104
	v_div_fixup_f32 v96, v97, v96, v115
	v_mul_f32_e32 v102, v99, v96
	v_mul_f32_e32 v96, 0xbfb8aa3b, v119
	v_exp_f32_e32 v96, v96
	s_nop 0
	v_add_f32_e32 v96, 1.0, v96
	v_div_scale_f32 v97, s[42:43], v96, v96, v119
	v_rcp_f32_e32 v98, v97
	s_nop 0
	v_fma_f32 v99, -v97, v98, 1.0
	v_fmac_f32_e32 v98, v99, v98
	v_div_scale_f32 v99, vcc, v119, v96, v119
	v_mul_f32_e32 v104, v99, v98
	v_fma_f32 v105, -v97, v104, v99
	v_fmac_f32_e32 v104, v105, v98
	v_fma_f32 v97, -v97, v104, v99
	v_div_fmas_f32 v97, v97, v98, v104
	v_div_fixup_f32 v96, v97, v96, v119
	v_mul_f32_e32 v103, v103, v96
	v_mul_f32_e32 v96, 0xbfb8aa3b, v123
	v_exp_f32_e32 v96, v96
	s_nop 0
	v_add_f32_e32 v96, 1.0, v96
	v_div_scale_f32 v97, s[42:43], v96, v96, v123
	v_rcp_f32_e32 v98, v97
	s_nop 0
	v_fma_f32 v99, -v97, v98, 1.0
	v_fmac_f32_e32 v98, v99, v98
	v_div_scale_f32 v99, vcc, v123, v96, v123
	v_mul_f32_e32 v104, v99, v98
	v_fma_f32 v105, -v97, v104, v99
	v_fmac_f32_e32 v104, v105, v98
	v_fma_f32 v97, -v97, v104, v99
	v_div_fmas_f32 v97, v97, v98, v104
	v_div_fixup_f32 v96, v97, v96, v123
	v_mul_f32_e32 v104, v107, v96
	v_mul_f32_e32 v96, 0xbfb8aa3b, v127
	v_exp_f32_e32 v96, v96
	s_nop 0
	v_add_f32_e32 v96, 1.0, v96
	v_div_scale_f32 v97, s[42:43], v96, v96, v127
	v_rcp_f32_e32 v98, v97
	s_nop 0
	v_fma_f32 v99, -v97, v98, 1.0
	v_fmac_f32_e32 v98, v99, v98
	v_div_scale_f32 v99, vcc, v127, v96, v127
	v_mul_f32_e32 v105, v99, v98
	v_fma_f32 v106, -v97, v105, v99
	v_fmac_f32_e32 v105, v106, v98
	v_fma_f32 v97, -v97, v105, v99
	v_div_fmas_f32 v97, v97, v98, v105
	v_div_fixup_f32 v96, v97, v96, v127
	v_mul_f32_e32 v105, v111, v96
	v_mov_b32_e32 v96, v1
	v_mov_b32_e32 v97, v1
	v_mov_b32_e32 v98, v1
	v_mov_b32_e32 v99, v1
	v_cvt_pk_fp8_f32 v96, v0, v7
	v_cvt_pk_fp8_f32 v97, v10, v11
	v_cvt_pk_fp8_f32 v98, v14, v15
	v_cvt_pk_fp8_f32 v99, v102, v103
	v_cvt_pk_fp8_f32 v96, v8, v9 op_sel:[0,0,1]
	v_cvt_pk_fp8_f32 v97, v12, v13 op_sel:[0,0,1]
	v_cvt_pk_fp8_f32 v98, v100, v101 op_sel:[0,0,1]
	v_cvt_pk_fp8_f32 v99, v104, v105 op_sel:[0,0,1]
	s_andn2_b64 vcc, exec, s[44:45]
	global_store_dwordx4 v[4:5], v[96:99], off offset:32
	s_cbranch_vccnz .LBB0_1314
	ds_read_b32 v0, v6 offset:55424
	s_waitcnt lgkmcnt(0)
	v_lshlrev_b64 v[4:5], 8, v[0:1]
	v_mul_f32_e32 v0, 0xbfb8aa3b, v80
	v_exp_f32_e32 v0, v0
	v_lshl_add_u64 v[2:3], v[2:3], 0, v[4:5]
	v_add_f32_e32 v0, 1.0, v0
	v_div_scale_f32 v4, s[42:43], v0, v0, v80
	v_rcp_f32_e32 v5, v4
	s_nop 0
	v_fma_f32 v6, -v4, v5, 1.0
	v_fmac_f32_e32 v5, v6, v5
	v_div_scale_f32 v6, vcc, v80, v0, v80
	v_mul_f32_e32 v7, v6, v5
	v_fma_f32 v8, -v4, v7, v6
	v_fmac_f32_e32 v7, v8, v5
	v_fma_f32 v4, -v4, v7, v6
	v_div_fmas_f32 v4, v4, v5, v7
	v_div_fixup_f32 v0, v4, v0, v80
	v_mul_f32_e32 v4, 0xbfb8aa3b, v84
	v_exp_f32_e32 v4, v4
	v_mul_f32_e32 v0, v64, v0
	v_add_f32_e32 v4, 1.0, v4
	v_div_scale_f32 v5, s[42:43], v4, v4, v84
	v_rcp_f32_e32 v6, v5
	s_nop 0
	v_fma_f32 v7, -v5, v6, 1.0
	v_fmac_f32_e32 v6, v7, v6
	v_div_scale_f32 v7, vcc, v84, v4, v84
	v_mul_f32_e32 v8, v7, v6
	v_fma_f32 v9, -v5, v8, v7
	v_fmac_f32_e32 v8, v9, v6
	v_fma_f32 v5, -v5, v8, v7
	v_div_fmas_f32 v5, v5, v6, v8
	v_div_fixup_f32 v4, v5, v4, v84
	v_mul_f32_e32 v5, 0xbfb8aa3b, v88
	v_exp_f32_e32 v5, v5
	v_mul_f32_e32 v4, v68, v4
	v_add_f32_e32 v5, 1.0, v5
	v_div_scale_f32 v6, s[42:43], v5, v5, v88
	v_rcp_f32_e32 v7, v6
	s_nop 0
	v_fma_f32 v8, -v6, v7, 1.0
	v_fmac_f32_e32 v7, v8, v7
	v_div_scale_f32 v8, vcc, v88, v5, v88
	v_mul_f32_e32 v9, v8, v7
	v_fma_f32 v10, -v6, v9, v8
	v_fmac_f32_e32 v9, v10, v7
	v_fma_f32 v6, -v6, v9, v8
	v_div_fmas_f32 v6, v6, v7, v9
	v_div_fixup_f32 v5, v6, v5, v88
	v_mul_f32_e32 v6, 0xbfb8aa3b, v92
	v_exp_f32_e32 v6, v6
	v_mul_f32_e32 v5, v72, v5
	v_add_f32_e32 v6, 1.0, v6
	v_div_scale_f32 v7, s[42:43], v6, v6, v92
	v_rcp_f32_e32 v8, v7
	s_nop 0
	v_fma_f32 v9, -v7, v8, 1.0
	v_fmac_f32_e32 v8, v9, v8
	v_div_scale_f32 v9, vcc, v92, v6, v92
	v_mul_f32_e32 v10, v9, v8
	v_fma_f32 v11, -v7, v10, v9
	v_fmac_f32_e32 v10, v11, v8
	v_fma_f32 v7, -v7, v10, v9
	v_div_fmas_f32 v7, v7, v8, v10
	v_div_fixup_f32 v6, v7, v6, v92
	v_mul_f32_e32 v7, 0xbfb8aa3b, v81
	v_exp_f32_e32 v7, v7
	v_mul_f32_e32 v6, v76, v6
	v_add_f32_e32 v7, 1.0, v7
	v_div_scale_f32 v8, s[42:43], v7, v7, v81
	v_rcp_f32_e32 v9, v8
	s_nop 0
	v_fma_f32 v10, -v8, v9, 1.0
	v_fmac_f32_e32 v9, v10, v9
	v_div_scale_f32 v10, vcc, v81, v7, v81
	v_mul_f32_e32 v11, v10, v9
	v_fma_f32 v12, -v8, v11, v10
	v_fmac_f32_e32 v11, v12, v9
	v_fma_f32 v8, -v8, v11, v10
	v_div_fmas_f32 v8, v8, v9, v11
	v_div_fixup_f32 v7, v8, v7, v81
	v_mul_f32_e32 v8, 0xbfb8aa3b, v85
	v_exp_f32_e32 v8, v8
	v_mul_f32_e32 v7, v65, v7
	v_add_f32_e32 v8, 1.0, v8
	v_div_scale_f32 v9, s[42:43], v8, v8, v85
	v_rcp_f32_e32 v10, v9
	s_nop 0
	v_fma_f32 v11, -v9, v10, 1.0
	v_fmac_f32_e32 v10, v11, v10
	v_div_scale_f32 v11, vcc, v85, v8, v85
	v_mul_f32_e32 v12, v11, v10
	v_fma_f32 v13, -v9, v12, v11
	v_fmac_f32_e32 v12, v13, v10
	v_fma_f32 v9, -v9, v12, v11
	v_div_fmas_f32 v9, v9, v10, v12
	v_div_fixup_f32 v8, v9, v8, v85
	v_mul_f32_e32 v9, 0xbfb8aa3b, v89
	v_exp_f32_e32 v9, v9
	v_mul_f32_e32 v8, v69, v8
	v_add_f32_e32 v9, 1.0, v9
	v_div_scale_f32 v10, s[42:43], v9, v9, v89
	v_rcp_f32_e32 v11, v10
	s_nop 0
	v_fma_f32 v12, -v10, v11, 1.0
	v_fmac_f32_e32 v11, v12, v11
	v_div_scale_f32 v12, vcc, v89, v9, v89
	v_mul_f32_e32 v13, v12, v11
	v_fma_f32 v14, -v10, v13, v12
	v_fmac_f32_e32 v13, v14, v11
	v_fma_f32 v10, -v10, v13, v12
	v_div_fmas_f32 v10, v10, v11, v13
	v_div_fixup_f32 v9, v10, v9, v89
	v_mul_f32_e32 v10, 0xbfb8aa3b, v93
	v_exp_f32_e32 v10, v10
	v_mul_f32_e32 v9, v73, v9
	v_add_f32_e32 v10, 1.0, v10
	v_div_scale_f32 v11, s[42:43], v10, v10, v93
	v_rcp_f32_e32 v12, v11
	s_nop 0
	v_fma_f32 v13, -v11, v12, 1.0
	v_fmac_f32_e32 v12, v13, v12
	v_div_scale_f32 v13, vcc, v93, v10, v93
	v_mul_f32_e32 v14, v13, v12
	v_fma_f32 v15, -v11, v14, v13
	v_fmac_f32_e32 v14, v15, v12
	v_fma_f32 v11, -v11, v14, v13
	v_div_fmas_f32 v11, v11, v12, v14
	v_div_fixup_f32 v10, v11, v10, v93
	v_mul_f32_e32 v11, 0xbfb8aa3b, v82
	v_exp_f32_e32 v11, v11
	v_mul_f32_e32 v10, v77, v10
	v_add_f32_e32 v11, 1.0, v11
	v_div_scale_f32 v12, s[42:43], v11, v11, v82
	v_rcp_f32_e32 v13, v12
	s_nop 0
	v_fma_f32 v14, -v12, v13, 1.0
	v_fmac_f32_e32 v13, v14, v13
	v_div_scale_f32 v14, vcc, v82, v11, v82
	v_mul_f32_e32 v15, v14, v13
	v_fma_f32 v64, -v12, v15, v14
	v_fmac_f32_e32 v15, v64, v13
	v_fma_f32 v12, -v12, v15, v14
	v_div_fmas_f32 v12, v12, v13, v15
	v_div_fixup_f32 v11, v12, v11, v82
	v_mul_f32_e32 v12, 0xbfb8aa3b, v86
	v_exp_f32_e32 v12, v12
	v_mul_f32_e32 v11, v66, v11
	v_add_f32_e32 v12, 1.0, v12
	v_div_scale_f32 v13, s[42:43], v12, v12, v86
	v_rcp_f32_e32 v14, v13
	s_nop 0
	v_fma_f32 v15, -v13, v14, 1.0
	v_fmac_f32_e32 v14, v15, v14
	v_div_scale_f32 v15, vcc, v86, v12, v86
	v_mul_f32_e32 v64, v15, v14
	v_fma_f32 v65, -v13, v64, v15
	v_fmac_f32_e32 v64, v65, v14
	v_fma_f32 v13, -v13, v64, v15
	v_div_fmas_f32 v13, v13, v14, v64
	v_div_fixup_f32 v12, v13, v12, v86
	v_mul_f32_e32 v15, v70, v12
	v_mul_f32_e32 v12, 0xbfb8aa3b, v90
	v_exp_f32_e32 v12, v12
	s_nop 0
	v_add_f32_e32 v12, 1.0, v12
	v_div_scale_f32 v13, s[42:43], v12, v12, v90
	v_rcp_f32_e32 v14, v13
	s_nop 0
	v_fma_f32 v64, -v13, v14, 1.0
	v_fmac_f32_e32 v14, v64, v14
	v_div_scale_f32 v64, vcc, v90, v12, v90
	v_mul_f32_e32 v65, v64, v14
	v_fma_f32 v66, -v13, v65, v64
	v_fmac_f32_e32 v65, v66, v14
	v_fma_f32 v13, -v13, v65, v64
	v_div_fmas_f32 v13, v13, v14, v65
	v_div_fixup_f32 v12, v13, v12, v90
	v_mul_f32_e32 v64, v74, v12
	v_mul_f32_e32 v12, 0xbfb8aa3b, v94
	v_exp_f32_e32 v12, v12
	s_nop 0
	v_add_f32_e32 v12, 1.0, v12
	v_div_scale_f32 v13, s[42:43], v12, v12, v94
	v_rcp_f32_e32 v14, v13
	s_nop 0
	v_fma_f32 v65, -v13, v14, 1.0
	v_fmac_f32_e32 v14, v65, v14
	v_div_scale_f32 v65, vcc, v94, v12, v94
	v_mul_f32_e32 v66, v65, v14
	v_fma_f32 v68, -v13, v66, v65
	v_fmac_f32_e32 v66, v68, v14
	v_fma_f32 v13, -v13, v66, v65
	v_div_fmas_f32 v13, v13, v14, v66
	v_div_fixup_f32 v12, v13, v12, v94
	v_mul_f32_e32 v65, v78, v12
	v_mul_f32_e32 v12, 0xbfb8aa3b, v83
	v_exp_f32_e32 v12, v12
	s_nop 0
	v_add_f32_e32 v12, 1.0, v12
	v_div_scale_f32 v13, s[42:43], v12, v12, v83
	v_rcp_f32_e32 v14, v13
	s_nop 0
	v_fma_f32 v66, -v13, v14, 1.0
	v_fmac_f32_e32 v14, v66, v14
	v_div_scale_f32 v66, vcc, v83, v12, v83
	v_mul_f32_e32 v68, v66, v14
	v_fma_f32 v69, -v13, v68, v66
	v_fmac_f32_e32 v68, v69, v14
	v_fma_f32 v13, -v13, v68, v66
	v_div_fmas_f32 v13, v13, v14, v68
	v_div_fixup_f32 v12, v13, v12, v83
	v_mul_f32_e32 v66, v67, v12
	v_mul_f32_e32 v12, 0xbfb8aa3b, v87
	v_exp_f32_e32 v12, v12
	s_nop 0
	v_add_f32_e32 v12, 1.0, v12
	v_div_scale_f32 v13, s[42:43], v12, v12, v87
	v_rcp_f32_e32 v14, v13
	s_nop 0
	v_fma_f32 v67, -v13, v14, 1.0
	v_fmac_f32_e32 v14, v67, v14
	v_div_scale_f32 v67, vcc, v87, v12, v87
	v_mul_f32_e32 v68, v67, v14
	v_fma_f32 v69, -v13, v68, v67
	v_fmac_f32_e32 v68, v69, v14
	v_fma_f32 v13, -v13, v68, v67
	v_div_fmas_f32 v13, v13, v14, v68
	v_div_fixup_f32 v12, v13, v12, v87
	v_mul_f32_e32 v67, v71, v12
	v_mul_f32_e32 v12, 0xbfb8aa3b, v91
	v_exp_f32_e32 v12, v12
	s_nop 0
	v_add_f32_e32 v12, 1.0, v12
	v_div_scale_f32 v13, s[42:43], v12, v12, v91
	v_rcp_f32_e32 v14, v13
	s_nop 0
	v_fma_f32 v68, -v13, v14, 1.0
	v_fmac_f32_e32 v14, v68, v14
	v_div_scale_f32 v68, vcc, v91, v12, v91
	v_mul_f32_e32 v69, v68, v14
	v_fma_f32 v70, -v13, v69, v68
	v_fmac_f32_e32 v69, v70, v14
	v_fma_f32 v13, -v13, v69, v68
	v_div_fmas_f32 v13, v13, v14, v69
	v_div_fixup_f32 v12, v13, v12, v91
	v_mul_f32_e32 v68, v75, v12
	v_mul_f32_e32 v12, 0xbfb8aa3b, v95
	v_exp_f32_e32 v12, v12
	s_nop 0
	v_add_f32_e32 v12, 1.0, v12
	v_div_scale_f32 v13, s[42:43], v12, v12, v95
	v_rcp_f32_e32 v14, v13
	s_nop 0
	v_fma_f32 v69, -v13, v14, 1.0
	v_fmac_f32_e32 v14, v69, v14
	v_div_scale_f32 v69, vcc, v95, v12, v95
	v_mul_f32_e32 v70, v69, v14
	v_fma_f32 v71, -v13, v70, v69
	v_fmac_f32_e32 v70, v71, v14
	v_fma_f32 v13, -v13, v70, v69
	v_div_fmas_f32 v13, v13, v14, v70
	v_div_fixup_f32 v12, v13, v12, v95
	v_mul_f32_e32 v69, v79, v12
	v_mov_b32_e32 v12, v1
	v_cvt_pk_fp8_f32 v12, v0, v4
	v_mul_f32_e32 v0, 0xbfb8aa3b, v48
	v_exp_f32_e32 v0, v0
	v_mov_b32_e32 v13, v1
	v_cvt_pk_fp8_f32 v12, v5, v6 op_sel:[0,0,1]
	v_cvt_pk_fp8_f32 v13, v7, v8
	v_add_f32_e32 v0, 1.0, v0
	v_div_scale_f32 v4, s[42:43], v0, v0, v48
	v_rcp_f32_e32 v5, v4
	v_cvt_pk_fp8_f32 v13, v9, v10 op_sel:[0,0,1]
	v_mov_b32_e32 v14, v1
	v_cvt_pk_fp8_f32 v14, v11, v15
	v_fma_f32 v6, -v4, v5, 1.0
	v_fmac_f32_e32 v5, v6, v5
	v_div_scale_f32 v6, vcc, v48, v0, v48
	v_mul_f32_e32 v7, v6, v5
	v_fma_f32 v8, -v4, v7, v6
	v_fmac_f32_e32 v7, v8, v5
	v_fma_f32 v4, -v4, v7, v6
	v_div_fmas_f32 v4, v4, v5, v7
	v_div_fixup_f32 v0, v4, v0, v48
	v_mul_f32_e32 v4, 0xbfb8aa3b, v52
	v_exp_f32_e32 v4, v4
	v_mov_b32_e32 v15, v1
	v_cvt_pk_fp8_f32 v15, v66, v67
	v_cvt_pk_fp8_f32 v14, v64, v65 op_sel:[0,0,1]
	v_add_f32_e32 v4, 1.0, v4
	v_div_scale_f32 v5, s[42:43], v4, v4, v52
	v_rcp_f32_e32 v6, v5
	v_cvt_pk_fp8_f32 v15, v68, v69 op_sel:[0,0,1]
	v_mul_f32_e32 v0, v32, v0
	v_fma_f32 v7, -v5, v6, 1.0
	v_fmac_f32_e32 v6, v7, v6
	v_div_scale_f32 v7, vcc, v52, v4, v52
	v_mul_f32_e32 v8, v7, v6
	v_fma_f32 v9, -v5, v8, v7
	v_fmac_f32_e32 v8, v9, v6
	v_fma_f32 v5, -v5, v8, v7
	v_div_fmas_f32 v5, v5, v6, v8
	v_div_fixup_f32 v4, v5, v4, v52
	v_mul_f32_e32 v5, 0xbfb8aa3b, v56
	v_exp_f32_e32 v5, v5
	global_store_dwordx4 v[2:3], v[12:15], off
	v_mul_f32_e32 v4, v36, v4
	v_add_f32_e32 v5, 1.0, v5
	v_div_scale_f32 v6, s[42:43], v5, v5, v56
	v_rcp_f32_e32 v7, v6
	s_nop 0
	v_fma_f32 v8, -v6, v7, 1.0
	v_fmac_f32_e32 v7, v8, v7
	v_div_scale_f32 v8, vcc, v56, v5, v56
	v_mul_f32_e32 v9, v8, v7
	v_fma_f32 v10, -v6, v9, v8
	v_fmac_f32_e32 v9, v10, v7
	v_fma_f32 v6, -v6, v9, v8
	v_div_fmas_f32 v6, v6, v7, v9
	v_div_fixup_f32 v5, v6, v5, v56
	v_mul_f32_e32 v6, 0xbfb8aa3b, v60
	v_exp_f32_e32 v6, v6
	v_mul_f32_e32 v5, v40, v5
	v_add_f32_e32 v6, 1.0, v6
	v_div_scale_f32 v7, s[42:43], v6, v6, v60
	v_rcp_f32_e32 v8, v7
	s_nop 0
	v_fma_f32 v9, -v7, v8, 1.0
	v_fmac_f32_e32 v8, v9, v8
	v_div_scale_f32 v9, vcc, v60, v6, v60
	v_mul_f32_e32 v10, v9, v8
	v_fma_f32 v11, -v7, v10, v9
	v_fmac_f32_e32 v10, v11, v8
	v_fma_f32 v7, -v7, v10, v9
	v_div_fmas_f32 v7, v7, v8, v10
	v_div_fixup_f32 v6, v7, v6, v60
	v_mul_f32_e32 v7, 0xbfb8aa3b, v49
	v_exp_f32_e32 v7, v7
	v_mul_f32_e32 v6, v44, v6
	v_add_f32_e32 v7, 1.0, v7
	v_div_scale_f32 v8, s[42:43], v7, v7, v49
	v_rcp_f32_e32 v9, v8
	s_nop 0
	v_fma_f32 v10, -v8, v9, 1.0
	v_fmac_f32_e32 v9, v10, v9
	v_div_scale_f32 v10, vcc, v49, v7, v49
	v_mul_f32_e32 v11, v10, v9
	v_fma_f32 v12, -v8, v11, v10
	v_fmac_f32_e32 v11, v12, v9
	v_fma_f32 v8, -v8, v11, v10
	v_div_fmas_f32 v8, v8, v9, v11
	v_div_fixup_f32 v7, v8, v7, v49
	v_mul_f32_e32 v8, 0xbfb8aa3b, v53
	v_exp_f32_e32 v8, v8
	v_mul_f32_e32 v7, v33, v7
	v_add_f32_e32 v8, 1.0, v8
	v_div_scale_f32 v9, s[42:43], v8, v8, v53
	v_rcp_f32_e32 v10, v9
	s_nop 0
	v_fma_f32 v11, -v9, v10, 1.0
	v_fmac_f32_e32 v10, v11, v10
	v_div_scale_f32 v11, vcc, v53, v8, v53
	v_mul_f32_e32 v12, v11, v10
	v_fma_f32 v13, -v9, v12, v11
	v_fmac_f32_e32 v12, v13, v10
	v_fma_f32 v9, -v9, v12, v11
	v_div_fmas_f32 v9, v9, v10, v12
	v_div_fixup_f32 v8, v9, v8, v53
	v_mul_f32_e32 v9, 0xbfb8aa3b, v57
	v_exp_f32_e32 v9, v9
	v_mul_f32_e32 v8, v37, v8
	v_add_f32_e32 v9, 1.0, v9
	v_div_scale_f32 v10, s[42:43], v9, v9, v57
	v_rcp_f32_e32 v11, v10
	s_nop 0
	v_fma_f32 v12, -v10, v11, 1.0
	v_fmac_f32_e32 v11, v12, v11
	v_div_scale_f32 v12, vcc, v57, v9, v57
	v_mul_f32_e32 v13, v12, v11
	v_fma_f32 v14, -v10, v13, v12
	v_fmac_f32_e32 v13, v14, v11
	v_fma_f32 v10, -v10, v13, v12
	v_div_fmas_f32 v10, v10, v11, v13
	v_div_fixup_f32 v9, v10, v9, v57
	v_mul_f32_e32 v10, 0xbfb8aa3b, v61
	v_exp_f32_e32 v10, v10
	v_mul_f32_e32 v9, v41, v9
	v_add_f32_e32 v10, 1.0, v10
	v_div_scale_f32 v11, s[42:43], v10, v10, v61
	v_rcp_f32_e32 v12, v11
	s_nop 0
	v_fma_f32 v13, -v11, v12, 1.0
	v_fmac_f32_e32 v12, v13, v12
	v_div_scale_f32 v13, vcc, v61, v10, v61
	v_mul_f32_e32 v14, v13, v12
	v_fma_f32 v15, -v11, v14, v13
	v_fmac_f32_e32 v14, v15, v12
	v_fma_f32 v11, -v11, v14, v13
	v_div_fmas_f32 v11, v11, v12, v14
	v_div_fixup_f32 v10, v11, v10, v61
	v_mul_f32_e32 v11, 0xbfb8aa3b, v50
	v_exp_f32_e32 v11, v11
	v_mul_f32_e32 v10, v45, v10
	v_add_f32_e32 v11, 1.0, v11
	v_div_scale_f32 v12, s[42:43], v11, v11, v50
	v_rcp_f32_e32 v13, v12
	s_nop 0
	v_fma_f32 v14, -v12, v13, 1.0
	v_fmac_f32_e32 v13, v14, v13
	v_div_scale_f32 v14, vcc, v50, v11, v50
	v_mul_f32_e32 v15, v14, v13
	v_fma_f32 v32, -v12, v15, v14
	v_fmac_f32_e32 v15, v32, v13
	v_fma_f32 v12, -v12, v15, v14
	v_div_fmas_f32 v12, v12, v13, v15
	v_div_fixup_f32 v11, v12, v11, v50
	v_mul_f32_e32 v12, 0xbfb8aa3b, v54
	v_exp_f32_e32 v12, v12
	v_mul_f32_e32 v11, v34, v11
	v_add_f32_e32 v12, 1.0, v12
	v_div_scale_f32 v13, s[42:43], v12, v12, v54
	v_rcp_f32_e32 v14, v13
	s_nop 0
	v_fma_f32 v15, -v13, v14, 1.0
	v_fmac_f32_e32 v14, v15, v14
	v_div_scale_f32 v15, vcc, v54, v12, v54
	v_mul_f32_e32 v32, v15, v14
	v_fma_f32 v33, -v13, v32, v15
	v_fmac_f32_e32 v32, v33, v14
	v_fma_f32 v13, -v13, v32, v15
	v_div_fmas_f32 v13, v13, v14, v32
	v_div_fixup_f32 v12, v13, v12, v54
	v_mul_f32_e32 v15, v38, v12
	v_mul_f32_e32 v12, 0xbfb8aa3b, v58
	v_exp_f32_e32 v12, v12
	s_nop 0
	v_add_f32_e32 v12, 1.0, v12
	v_div_scale_f32 v13, s[42:43], v12, v12, v58
	v_rcp_f32_e32 v14, v13
	s_nop 0
	v_fma_f32 v32, -v13, v14, 1.0
	v_fmac_f32_e32 v14, v32, v14
	v_div_scale_f32 v32, vcc, v58, v12, v58
	v_mul_f32_e32 v33, v32, v14
	v_fma_f32 v34, -v13, v33, v32
	v_fmac_f32_e32 v33, v34, v14
	v_fma_f32 v13, -v13, v33, v32
	v_div_fmas_f32 v13, v13, v14, v33
	v_div_fixup_f32 v12, v13, v12, v58
	v_mul_f32_e32 v32, v42, v12
	v_mul_f32_e32 v12, 0xbfb8aa3b, v62
	v_exp_f32_e32 v12, v12
	s_nop 0
	v_add_f32_e32 v12, 1.0, v12
	v_div_scale_f32 v13, s[42:43], v12, v12, v62
	v_rcp_f32_e32 v14, v13
	s_nop 0
	v_fma_f32 v33, -v13, v14, 1.0
	v_fmac_f32_e32 v14, v33, v14
	v_div_scale_f32 v33, vcc, v62, v12, v62
	v_mul_f32_e32 v34, v33, v14
	v_fma_f32 v36, -v13, v34, v33
	v_fmac_f32_e32 v34, v36, v14
	v_fma_f32 v13, -v13, v34, v33
	v_div_fmas_f32 v13, v13, v14, v34
	v_div_fixup_f32 v12, v13, v12, v62
	v_mul_f32_e32 v33, v46, v12
	v_mul_f32_e32 v12, 0xbfb8aa3b, v51
	v_exp_f32_e32 v12, v12
	s_nop 0
	v_add_f32_e32 v12, 1.0, v12
	v_div_scale_f32 v13, s[42:43], v12, v12, v51
	v_rcp_f32_e32 v14, v13
	s_nop 0
	v_fma_f32 v34, -v13, v14, 1.0
	v_fmac_f32_e32 v14, v34, v14
	v_div_scale_f32 v34, vcc, v51, v12, v51
	v_mul_f32_e32 v36, v34, v14
	v_fma_f32 v37, -v13, v36, v34
	v_fmac_f32_e32 v36, v37, v14
	v_fma_f32 v13, -v13, v36, v34
	v_div_fmas_f32 v13, v13, v14, v36
	v_div_fixup_f32 v12, v13, v12, v51
	v_mul_f32_e32 v34, v35, v12
	v_mul_f32_e32 v12, 0xbfb8aa3b, v55
	v_exp_f32_e32 v12, v12
	s_nop 0
	v_add_f32_e32 v12, 1.0, v12
	v_div_scale_f32 v13, s[42:43], v12, v12, v55
	v_rcp_f32_e32 v14, v13
	s_nop 0
	v_fma_f32 v35, -v13, v14, 1.0
	v_fmac_f32_e32 v14, v35, v14
	v_div_scale_f32 v35, vcc, v55, v12, v55
	v_mul_f32_e32 v36, v35, v14
	v_fma_f32 v37, -v13, v36, v35
	v_fmac_f32_e32 v36, v37, v14
	v_fma_f32 v13, -v13, v36, v35
	v_div_fmas_f32 v13, v13, v14, v36
	v_div_fixup_f32 v12, v13, v12, v55
	v_mul_f32_e32 v35, v39, v12
	v_mul_f32_e32 v12, 0xbfb8aa3b, v59
	v_exp_f32_e32 v12, v12
	s_nop 0
	v_add_f32_e32 v12, 1.0, v12
	v_div_scale_f32 v13, s[42:43], v12, v12, v59
	v_rcp_f32_e32 v14, v13
	s_nop 0
	v_fma_f32 v36, -v13, v14, 1.0
	v_fmac_f32_e32 v14, v36, v14
	v_div_scale_f32 v36, vcc, v59, v12, v59
	v_mul_f32_e32 v37, v36, v14
	v_fma_f32 v38, -v13, v37, v36
	v_fmac_f32_e32 v37, v38, v14
	v_fma_f32 v13, -v13, v37, v36
	v_div_fmas_f32 v13, v13, v14, v37
	v_div_fixup_f32 v12, v13, v12, v59
	v_mul_f32_e32 v36, v43, v12
	v_mul_f32_e32 v12, 0xbfb8aa3b, v63
	v_exp_f32_e32 v12, v12
	s_nop 0
	v_add_f32_e32 v12, 1.0, v12
	v_div_scale_f32 v13, s[42:43], v12, v12, v63
	v_rcp_f32_e32 v14, v13
	s_nop 0
	v_fma_f32 v37, -v13, v14, 1.0
	v_fmac_f32_e32 v14, v37, v14
	v_div_scale_f32 v37, vcc, v63, v12, v63
	v_mul_f32_e32 v38, v37, v14
	v_fma_f32 v39, -v13, v38, v37
	v_fmac_f32_e32 v38, v39, v14
	v_fma_f32 v13, -v13, v38, v37
	v_div_fmas_f32 v13, v13, v14, v38
	v_div_fixup_f32 v12, v13, v12, v63
	v_mov_b32_e32 v14, v1
	v_mul_f32_e32 v37, v47, v12
	v_mov_b32_e32 v12, v1
	v_mov_b32_e32 v13, v1
	v_cvt_pk_fp8_f32 v14, v11, v15
	v_mov_b32_e32 v15, v1
	v_cvt_pk_fp8_f32 v12, v0, v4
	v_cvt_pk_fp8_f32 v13, v7, v8
	v_cvt_pk_fp8_f32 v15, v34, v35
	v_cvt_pk_fp8_f32 v14, v32, v33 op_sel:[0,0,1]
	v_cvt_pk_fp8_f32 v12, v5, v6 op_sel:[0,0,1]
	v_cvt_pk_fp8_f32 v13, v9, v10 op_sel:[0,0,1]
	v_cvt_pk_fp8_f32 v15, v36, v37 op_sel:[0,0,1]
	global_store_dwordx4 v[2:3], v[12:15], off offset:32

.LBB0_1319:
	s_waitcnt vmcnt(0)
	v_mov_b32_e32 v220, 0x7f79
	v_mov_b32_e32 v221, 1
	v_mov_b32_e32 v222, 0x7b79
	v_mov_b32_e32 v223, 0x3727c5ac
	v_mov_b32_e32 v224, 0x42800000
	v_mov_b32_e32 v225, 0xf149f2ca
	v_mov_b32_e32 v226, 0x41b17218
	v_mov_b32_e32 v227, 0x7f800000
	v_mov_b32_e32 v228, 0xff800000
	v_mov_b32_e32 v229, 0x63
	v_bfrev_b32_e32 v230, -2
	v_readlane_b32 s25, v253, 0
	v_mbcnt_lo_u32_b32 v231, -1, 0
	v_mbcnt_hi_u32_b32 v231, -1, v231
	s_nop 0
	v_add_u32_e32 v231, s25, v231
	s_mov_b64 s[0:1], 0
	s_barrier
